# v77 stack + MoE down-projection epilogue: lane pairs exchange halves so each 16-byte store instruction writes whole 32-byte sectors
# baseline (speedup 1.0000x reference)
.LBB0_906:
	s_getreg_b32 s6, hwreg(HW_REG_HW_ID, 0, 6)
	s_lshl_b32 s6, s6, 2
	s_add_i32 s6, s6, 0x27000
	v_mov_b32_e32 v52, s6
	ds_read_b32 v52, v52
	v_mov_b32_e32 v53, 0
	s_waitcnt vmcnt(7)
	v_cvt_pk_bf16_f32 v4, v4, v5
	v_mbcnt_lo_u32_b32 v53, -1, v53
	v_mbcnt_hi_u32_b32 v53, -1, v53
	s_waitcnt lgkmcnt(0)
	v_readfirstlane_b32 s6, v52
	v_cvt_pk_bf16_f32 v5, v6, v7
	s_waitcnt vmcnt(6)
	v_cvt_pk_bf16_f32 v0, v0, v1
	v_lshl_or_b32 v62, s6, 6, v53
	v_cvt_pk_bf16_f32 v1, v2, v3
	v_lshrrev_b32_e32 v53, 3, v62
	v_lshlrev_b32_e32 v54, 4, v62
	v_and_b32_e32 v68, 0x70, v54
	v_mul_lo_u32 v69, v53, s20
	v_ashrrev_i32_e32 v52, 5, v62
	v_add3_u32 v53, 0, v68, v69
	ds_write_b128 v53, v[32:35]
	ds_write_b128 v53, v[36:39] offset:9216
	ds_write_b128 v53, v[40:43] offset:18432
	s_waitcnt vmcnt(5)
	ds_write_b128 v53, v[44:47] offset:27648
	s_waitcnt vmcnt(4)
	ds_write_b128 v53, v[48:51] offset:36864
	v_lshrrev_b32_e32 v34, 1, v52
	v_bfe_u32 v32, v62, 2, 3
	v_and_b32_e32 v33, 3, v52
	v_and_b32_e32 v34, 4, v34
	v_bitop3_b32 v32, v34, v32, v33 bitop3:0x36
	v_lshlrev_b32_e32 v33, 2, v62
	v_and_b32_e32 v67, 12, v33
	v_lshlrev_b32_e32 v70, 1, v67
	v_lshl_or_b32 v130, v32, 5, v70
	v_lshlrev_b32_e32 v131, 8, v52
	v_add3_u32 v6, s21, v130, v131
	ds_write2st64_b64 v6, v[4:5], v[0:1] offset1:8
	s_waitcnt vmcnt(5)
	v_cvt_pk_bf16_f32 v0, v12, v13
	v_cvt_pk_bf16_f32 v1, v14, v15
	s_waitcnt vmcnt(4)
	v_cvt_pk_bf16_f32 v2, v8, v9
	v_cvt_pk_bf16_f32 v3, v10, v11
	ds_write2st64_b64 v6, v[0:1], v[2:3] offset0:16 offset1:24
	v_sub_u32_e32 v0, v156, v143
	v_xad_u32 v2, s14, -1, v0
	v_add_u32_e32 v1, s14, v141
	v_min_i32_e32 v0, 0, v2
	v_add_u32_e32 v3, v1, v143
	v_add_u32_e32 v0, v0, v3
	v_ashrrev_i32_e32 v1, 31, v0
	v_lshlrev_b64 v[0:1], 9, v[0:1]
	v_lshl_add_u64 v[52:53], v[134:135], 0, v[0:1]
	v_min_i32_e32 v0, 64, v2
	v_add_u32_e32 v0, v0, v3
	v_ashrrev_i32_e32 v1, 31, v0
	v_lshlrev_b64 v[0:1], 9, v[0:1]
	v_lshl_add_u64 v[54:55], v[134:135], 0, v[0:1]
	v_min_i32_e32 v0, 0x80, v2
	v_add_u32_e32 v0, v0, v3
	v_ashrrev_i32_e32 v1, 31, v0
	v_lshlrev_b64 v[0:1], 9, v[0:1]
	v_lshl_add_u64 v[56:57], v[134:135], 0, v[0:1]
	v_min_i32_e32 v0, 0xc0, v2
	v_add_u32_e32 v0, v0, v3
	v_ashrrev_i32_e32 v1, 31, v0
	v_lshlrev_b64 v[0:1], 9, v[0:1]
	v_lshl_add_u64 v[58:59], v[134:135], 0, v[0:1]
	v_min_i32_e32 v0, 0x100, v2
	v_add_u32_e32 v0, v0, v3
	v_ashrrev_i32_e32 v1, 31, v0
	v_lshlrev_b64 v[0:1], 9, v[0:1]
	v_lshl_add_u64 v[60:61], v[134:135], 0, v[0:1]
	v_lshrrev_b32_e32 v1, 2, v62
	v_bfe_u32 v65, v62, 2, 2
	v_and_b32_e32 v1, 4, v1
	v_bfe_u32 v66, v62, 6, 1
	v_lshrrev_b32_e32 v0, 1, v62
	v_or_b32_e32 v2, v1, v65
	v_and_b32_e32 v71, 24, v0
	v_lshlrev_b32_e32 v3, 6, v66
	v_lshlrev_b32_e32 v2, 4, v2
	s_cmpk_lt_i32 s13, 0x100
	v_readlane_b32 s44, v253, 4
	v_or_b32_e32 v0, v71, v65
	v_xor_b32_e32 v2, v2, v3
	s_cselect_b32 s6, s13, 0
	v_readlane_b32 s50, v253, 10
	v_readlane_b32 s51, v253, 11
	v_readlane_b32 s56, v253, 16
	v_readlane_b32 s57, v253, 17
	v_or_b32_e32 v2, v2, v67
	v_lshlrev_b32_e32 v72, 8, v0
	v_lshlrev_b32_e32 v0, 2, v66
	s_cselect_b32 s9, s51, s57
	s_cselect_b32 s8, s50, s56
	s_ashr_i32 s7, s6, 31
	v_lshlrev_b32_e32 v192, 1, v2
	v_or_b32_e32 v2, 1, v0
	s_lshl_b64 s[6:7], s[6:7], 20
	v_bitop3_b32 v2, v1, v2, v65 bitop3:0x36
	s_add_u32 s8, s8, s6
	v_lshl_or_b32 v196, v2, 5, v70
	v_or_b32_e32 v2, 2, v0
	v_or_b32_e32 v0, 3, v0
	s_addc_u32 s9, s9, s7
	s_lshl_b32 s6, s15, 7
	v_bitop3_b32 v0, v1, v0, v65 bitop3:0x36
	s_ashr_i32 s7, s6, 31
	v_bitop3_b32 v2, v1, v2, v65 bitop3:0x36
	v_lshl_or_b32 v200, v0, 5, v70
	v_lshl_add_u64 v[0:1], s[8:9], 0, v[144:145]
	s_lshl_b64 s[10:11], s[6:7], 2
	v_lshl_add_u64 v[0:1], v[0:1], 0, s[10:11]
	v_lshl_add_u64 v[0:1], v[0:1], 0, v[132:133]
	v_mov_b32_e32 v149, v133
	v_lshl_add_u64 v[0:1], v[0:1], 0, v[148:149]
	v_mov_b32_e32 v151, v133
	v_lshl_add_u64 v[0:1], v[0:1], 0, v[150:151]
	v_lshl_or_b32 v197, v2, 5, v70
	v_add_co_u32_e32 v2, vcc, s16, v0
	global_load_dwordx4 v[32:35], v[52:53], off offset:128
	global_load_dwordx4 v[36:39], v[54:55], off offset:128
	v_addc_co_u32_e32 v3, vcc, 0, v1, vcc
	global_load_dwordx4 v[40:43], v[56:57], off offset:128
	global_load_dwordx4 v[44:47], v[58:59], off offset:128
	global_load_dwordx4 v[48:51], v[60:61], off offset:128
	s_waitcnt lgkmcnt(0)
	s_barrier
	global_load_dwordx4 v[12:15], v[0:1], off
	global_load_dwordx4 v[8:11], v[2:3], off
	v_add_co_u32_e32 v2, vcc, s17, v0
	v_ashrrev_i32_e32 v63, 7, v62
	s_nop 0
	v_addc_co_u32_e32 v3, vcc, 0, v1, vcc
	v_add_co_u32_e32 v0, vcc, s18, v0
	v_and_b32_e32 v64, 15, v62
	s_nop 0
	v_addc_co_u32_e32 v1, vcc, 0, v1, vcc
	global_load_dwordx4 v[4:7], v[2:3], off
	s_nop 0
	global_load_dwordx4 v[0:3], v[0:1], off
	v_add_u32_e32 v62, s21, v72
	v_add_u32_e32 v81, v62, v192
	v_add_u32_e32 v83, v62, v196
	v_add_u32_e32 v79, v62, v197
	v_add_u32_e32 v100, v62, v200
	v_mul_lo_u32 v62, v63, s19
	v_add_u32_e32 v193, 0, v72
	v_or_b32_e32 v62, v62, v64
	v_add_u32_e32 v67, 0x16c00, v193
	v_lshlrev_b32_e32 v63, 1, v71
	v_mul_lo_u32 v62, v62, s20
	v_add_u32_e32 v82, v67, v192
	v_add_u32_e32 v84, v67, v196
	v_add_u32_e32 v80, v67, v197
	v_add_u32_e32 v101, v67, v200
	v_add3_u32 v62, 0, v63, v62
	ds_read_b64_tr_b16 v[102:103], v81
	ds_read_b64_tr_b16 v[104:105], v82
	ds_read_b64_tr_b16 v[106:107], v83
	ds_read_b64_tr_b16 v[108:109], v84
	ds_read_b128 v[64:67], v62
	ds_read_b64_tr_b16 v[110:111], v79
	ds_read_b64_tr_b16 v[112:113], v80
	ds_read_b128 v[114:117], v62 offset:2304
	ds_read_b64_tr_b16 v[122:123], v100
	ds_read_b64_tr_b16 v[124:125], v101
	s_waitcnt lgkmcnt(5)
	v_mfma_f32_16x16x32_bf16 v[118:121], v[102:105], v[64:67], 0
	v_add3_u32 v63, 0, v131, v130
	v_or_b32_e32 v201, 0x2000, v72
	v_add_u32_e32 v70, 0x18c00, v193
	v_mfma_f32_16x16x32_bf16 v[126:129], v[106:109], v[64:67], 0
	v_add3_u32 v86, 0, v69, v68
	v_add_u32_e32 v68, s22, v72
	ds_read_b128 v[180:183], v62 offset:4608
	ds_read_b128 v[184:187], v62 offset:6912
	s_waitcnt lgkmcnt(5)
	v_mfma_f32_16x16x32_bf16 v[152:155], v[110:113], v[64:67], 0
	v_add_u32_e32 v98, 0x1b800, v63
	v_add_u32_e32 v95, 0x1c800, v63
	v_add_u32_e32 v92, 0x1d800, v63
	s_waitcnt lgkmcnt(2)
	v_mfma_f32_16x16x32_bf16 v[164:167], v[122:125], v[64:67], 0
	v_add_u32_e32 v64, 0x1ac00, v193
	v_add_u32_e32 v78, v64, v192
	v_add_u32_e32 v75, v64, v196
	v_add_u32_e32 v73, v64, v197
	v_add_u32_e32 v72, v64, v200
	v_add_u32_e32 v64, 0x1cc00, v193
	v_add3_u32 v91, s21, v192, v201
	v_add_u32_e32 v93, v70, v192
	v_add3_u32 v89, s21, v196, v201
	v_add_u32_e32 v90, v70, v196
	v_add3_u32 v85, s21, v197, v201
	v_add_u32_e32 v94, v70, v197
	v_add3_u32 v96, s21, v200, v201
	v_add_u32_e32 v97, v70, v200
	v_add_u32_e32 v77, v68, v192
	v_add_u32_e32 v74, v68, v196
	v_mfma_f32_16x16x32_bf16 v[168:171], v[102:105], v[114:117], 0
	v_add_u32_e32 v76, v68, v197
	v_add_u32_e32 v71, v68, v200
	v_add_u32_e32 v241, 0x17800, v63
	v_mfma_f32_16x16x32_bf16 v[172:175], v[106:109], v[114:117], 0
	v_add_u32_e32 v242, 0x18800, v63
	v_add_u32_e32 v243, 0x19800, v63
	v_add3_u32 v68, s22, v192, v201
	v_mfma_f32_16x16x32_bf16 v[176:179], v[110:113], v[114:117], 0
	v_add_u32_e32 v70, v64, v192
	v_add3_u32 v67, s22, v196, v201
	v_add_u32_e32 v69, v64, v196
	v_mfma_f32_16x16x32_bf16 v[114:117], v[122:125], v[114:117], 0
	v_add3_u32 v65, s22, v197, v201
	v_add_u32_e32 v66, v64, v197
	v_add3_u32 v63, s22, v200, v201
	v_add_u32_e32 v64, v64, v200
	ds_read_b128 v[200:203], v62 offset:9216
	v_add3_u32 v99, s22, v131, v130
	v_add_u32_e32 v87, 0x12000, v86
	v_add_u32_e32 v88, 0x14400, v86
	s_waitcnt vmcnt(12)
	v_cvt_pk_bf16_f32 v28, v28, v29
	v_cvt_pk_bf16_f32 v29, v30, v31
	s_waitcnt vmcnt(11)
	v_cvt_pk_bf16_f32 v24, v24, v25
	v_cvt_pk_bf16_f32 v25, v26, v27
	v_readlane_b32 s45, v253, 5
	v_readlane_b32 s46, v253, 6
	v_readlane_b32 s47, v253, 7
	v_readlane_b32 s48, v253, 8
	v_readlane_b32 s49, v253, 9
	v_readlane_b32 s52, v253, 12
	v_readlane_b32 s53, v253, 13
	v_readlane_b32 s54, v253, 14
	v_readlane_b32 s55, v253, 15
	v_readlane_b32 s58, v253, 18
	v_readlane_b32 s59, v253, 19
	v_add3_u32 v240, s21, v131, v130
	s_waitcnt lgkmcnt(2)
	v_mfma_f32_16x16x32_bf16 v[188:191], v[102:105], v[180:183], 0
	ds_write_b64 v99, v[28:29]
	ds_write_b64 v98, v[24:25]
	v_mfma_f32_16x16x32_bf16 v[192:195], v[106:109], v[180:183], 0
	v_mfma_f32_16x16x32_bf16 v[196:199], v[110:113], v[180:183], 0
	v_mfma_f32_16x16x32_bf16 v[180:183], v[122:125], v[180:183], 0
	ds_read_b128 v[208:211], v62 offset:64
	ds_read_b128 v[212:215], v62 offset:2368
	s_waitcnt vmcnt(9)
	v_cvt_pk_bf16_f32 v16, v16, v17
	v_cvt_pk_bf16_f32 v17, v18, v19
	s_waitcnt lgkmcnt(5)
	v_mfma_f32_16x16x32_bf16 v[24:27], v[102:105], v[184:187], 0
	ds_read_b128 v[216:219], v62 offset:4672
	v_cvt_pk_bf16_f32 v130, v20, v21
	v_cvt_pk_bf16_f32 v131, v22, v23
	v_mfma_f32_16x16x32_bf16 v[28:31], v[106:109], v[184:187], 0
	ds_write_b64 v92, v[16:17]
	ds_write_b64 v95, v[130:131]
	s_waitcnt lgkmcnt(7)
	v_mfma_f32_16x16x32_bf16 v[102:105], v[102:105], v[200:203], 0
	v_mfma_f32_16x16x32_bf16 v[106:109], v[106:109], v[200:203], 0
	v_mfma_f32_16x16x32_bf16 v[20:23], v[110:113], v[200:203], 0
	v_mfma_f32_16x16x32_bf16 v[16:19], v[122:125], v[200:203], 0
	v_mfma_f32_16x16x32_bf16 v[204:207], v[110:113], v[184:187], 0
	v_mfma_f32_16x16x32_bf16 v[184:187], v[122:125], v[184:187], 0
	ds_read_b64_tr_b16 v[110:111], v91
	ds_read_b64_tr_b16 v[112:113], v93
	ds_read_b64_tr_b16 v[122:123], v89
	ds_read_b64_tr_b16 v[124:125], v90
	ds_read_b64_tr_b16 v[200:201], v85
	ds_read_b64_tr_b16 v[202:203], v94
	ds_read_b64_tr_b16 v[220:221], v96
	ds_read_b64_tr_b16 v[222:223], v97
	s_waitcnt lgkmcnt(6)
	v_mfma_f32_16x16x32_bf16 v[118:121], v[110:113], v[208:211], v[118:121]
	s_waitcnt lgkmcnt(4)
	v_mfma_f32_16x16x32_bf16 v[126:129], v[122:125], v[208:211], v[126:129]
	s_waitcnt lgkmcnt(2)
	v_mfma_f32_16x16x32_bf16 v[152:155], v[200:203], v[208:211], v[152:155]
	s_waitcnt lgkmcnt(0)
	v_mfma_f32_16x16x32_bf16 v[164:167], v[220:223], v[208:211], v[164:167]
	v_mfma_f32_16x16x32_bf16 v[168:171], v[110:113], v[212:215], v[168:171]
	v_mfma_f32_16x16x32_bf16 v[172:175], v[122:125], v[212:215], v[172:175]
	v_mfma_f32_16x16x32_bf16 v[176:179], v[200:203], v[212:215], v[176:179]
	v_mfma_f32_16x16x32_bf16 v[114:117], v[220:223], v[212:215], v[114:117]
	ds_read_b128 v[208:211], v62 offset:6976
	ds_read_b128 v[212:215], v62 offset:9280
	s_waitcnt vmcnt(8)
	ds_write_b128 v86, v[32:35] offset:46080
	s_waitcnt vmcnt(7)
	ds_write_b128 v86, v[36:39] offset:55296
	v_mfma_f32_16x16x32_bf16 v[32:35], v[220:223], v[216:219], v[180:183]
	v_mfma_f32_16x16x32_bf16 v[188:191], v[110:113], v[216:219], v[188:191]
	v_mfma_f32_16x16x32_bf16 v[192:195], v[122:125], v[216:219], v[192:195]
	v_mfma_f32_16x16x32_bf16 v[196:199], v[200:203], v[216:219], v[196:199]
	s_waitcnt vmcnt(6)
	ds_write_b128 v86, v[40:43] offset:64512
	s_waitcnt vmcnt(5)
	ds_write_b128 v87, v[44:47]
	s_waitcnt vmcnt(4)
	ds_write_b128 v88, v[48:51]
	s_waitcnt lgkmcnt(6)
	v_mfma_f32_16x16x32_bf16 v[36:39], v[110:113], v[208:211], v[24:27]
	v_mfma_f32_16x16x32_bf16 v[180:183], v[122:125], v[208:211], v[28:31]
	v_mfma_f32_16x16x32_bf16 v[204:207], v[200:203], v[208:211], v[204:207]
	v_mfma_f32_16x16x32_bf16 v[184:187], v[220:223], v[208:211], v[184:187]
	s_waitcnt lgkmcnt(5)
	v_mfma_f32_16x16x32_bf16 v[102:105], v[110:113], v[212:215], v[102:105]
	v_mfma_f32_16x16x32_bf16 v[110:113], v[200:203], v[212:215], v[20:23]
	global_load_dwordx4 v[40:43], v[52:53], off offset:256
	global_load_dwordx4 v[44:47], v[54:55], off offset:256
	global_load_dwordx4 v[48:51], v[56:57], off offset:256
	global_load_dwordx4 v[200:203], v[58:59], off offset:256
	global_load_dwordx4 v[208:211], v[60:61], off offset:256
	v_mfma_f32_16x16x32_bf16 v[106:109], v[122:125], v[212:215], v[106:109]
	v_mfma_f32_16x16x32_bf16 v[122:125], v[220:223], v[212:215], v[16:19]
	s_waitcnt lgkmcnt(0)
	s_barrier
	ds_read_b64_tr_b16 v[212:213], v77
	ds_read_b64_tr_b16 v[214:215], v78
	ds_read_b128 v[16:19], v62 offset:46080
	ds_read_b64_tr_b16 v[216:217], v74
	ds_read_b64_tr_b16 v[218:219], v75
	ds_read_b64_tr_b16 v[220:221], v76
	ds_read_b128 v[20:23], v62 offset:48384
	ds_read_b128 v[224:227], v62 offset:55296
	ds_read_b64_tr_b16 v[222:223], v73
	ds_read_b64_tr_b16 v[228:229], v71
	ds_read_b64_tr_b16 v[230:231], v72
	s_waitcnt lgkmcnt(8)
	v_mfma_f32_16x16x32_bf16 v[118:121], v[212:215], v[16:19], v[118:121]
	ds_read_b128 v[232:235], v62 offset:50688
	s_waitcnt vmcnt(8)
	v_cvt_pk_bf16_f32 v12, v12, v13
	v_cvt_pk_bf16_f32 v13, v14, v15
	s_waitcnt lgkmcnt(7)
	v_mfma_f32_16x16x32_bf16 v[126:129], v[216:219], v[16:19], v[126:129]
	s_waitcnt vmcnt(7)
	v_cvt_pk_bf16_f32 v8, v8, v9
	v_cvt_pk_bf16_f32 v9, v10, v11
	s_waitcnt lgkmcnt(3)
	v_mfma_f32_16x16x32_bf16 v[152:155], v[220:223], v[16:19], v[152:155]
	s_waitcnt lgkmcnt(1)
	v_mfma_f32_16x16x32_bf16 v[164:167], v[228:231], v[16:19], v[164:167]
	v_lshl_add_u64 v[16:17], s[8:9], 0, v[146:147]
	v_lshl_add_u64 v[16:17], v[16:17], 0, s[10:11]
	v_lshl_add_u64 v[16:17], v[16:17], 0, v[132:133]
	v_lshl_add_u64 v[16:17], v[16:17], 0, v[148:149]
	v_lshl_add_u64 v[16:17], v[16:17], 0, v[150:151]
	v_add_co_u32_e32 v18, vcc, s16, v16
	v_mfma_f32_16x16x32_bf16 v[168:171], v[212:215], v[20:23], v[168:171]
	s_nop 0
	v_addc_co_u32_e32 v19, vcc, 0, v17, vcc
	global_load_dwordx4 v[28:31], v[16:17], off
	global_load_dwordx4 v[24:27], v[18:19], off
	v_add_co_u32_e32 v18, vcc, s17, v16
	v_mfma_f32_16x16x32_bf16 v[172:175], v[216:219], v[20:23], v[172:175]
	s_nop 0
	v_addc_co_u32_e32 v19, vcc, 0, v17, vcc
	v_add_co_u32_e32 v16, vcc, s18, v16
	v_mfma_f32_16x16x32_bf16 v[176:179], v[220:223], v[20:23], v[176:179]
	s_nop 0
	v_addc_co_u32_e32 v17, vcc, 0, v17, vcc
	ds_read_b128 v[236:239], v62 offset:52992
	v_mfma_f32_16x16x32_bf16 v[114:117], v[228:231], v[20:23], v[114:117]
	global_load_dwordx4 v[20:23], v[18:19], off
	s_nop 0
	global_load_dwordx4 v[16:19], v[16:17], off
	ds_write_b64 v240, v[12:13]
	ds_write_b64 v241, v[8:9]
	s_waitcnt lgkmcnt(3)
	v_mfma_f32_16x16x32_bf16 v[32:35], v[228:231], v[232:235], v[32:35]
	v_mfma_f32_16x16x32_bf16 v[188:191], v[212:215], v[232:235], v[188:191]
	v_mfma_f32_16x16x32_bf16 v[192:195], v[216:219], v[232:235], v[192:195]
	v_mfma_f32_16x16x32_bf16 v[196:199], v[220:223], v[232:235], v[196:199]
	s_waitcnt lgkmcnt(2)
	v_mfma_f32_16x16x32_bf16 v[8:11], v[212:215], v[236:239], v[36:39]
	s_waitcnt vmcnt(9)
	v_cvt_pk_bf16_f32 v0, v0, v1
	v_cvt_pk_bf16_f32 v1, v2, v3
	v_cvt_pk_bf16_f32 v130, v4, v5
	v_mfma_f32_16x16x32_bf16 v[12:15], v[216:219], v[236:239], v[180:183]
	v_cvt_pk_bf16_f32 v131, v6, v7
	v_mfma_f32_16x16x32_bf16 v[36:39], v[220:223], v[236:239], v[204:207]
	v_mfma_f32_16x16x32_bf16 v[180:183], v[228:231], v[236:239], v[184:187]
	s_nop 2
	ds_read_b128 v[184:187], v62 offset:46144
	ds_read_b128 v[204:207], v62 offset:48448
	v_mfma_f32_16x16x32_bf16 v[102:105], v[212:215], v[224:227], v[102:105]
	ds_read_b128 v[212:215], v62 offset:50752
	ds_write_b64 v243, v[0:1]
	ds_write_b64 v242, v[130:131]
	v_mfma_f32_16x16x32_bf16 v[106:109], v[216:219], v[224:227], v[106:109]
	v_mfma_f32_16x16x32_bf16 v[4:7], v[220:223], v[224:227], v[110:113]
	v_mfma_f32_16x16x32_bf16 v[0:3], v[228:231], v[224:227], v[122:125]
	s_nop 1
	ds_read_b64_tr_b16 v[110:111], v68
	ds_read_b64_tr_b16 v[112:113], v70
	ds_read_b64_tr_b16 v[122:123], v67
	ds_read_b64_tr_b16 v[124:125], v69
	ds_read_b64_tr_b16 v[216:217], v65
	ds_read_b64_tr_b16 v[218:219], v66
	ds_read_b64_tr_b16 v[220:221], v63
	ds_read_b64_tr_b16 v[222:223], v64
	s_waitcnt lgkmcnt(6)
	v_mfma_f32_16x16x32_bf16 v[118:121], v[110:113], v[184:187], v[118:121]
	s_waitcnt lgkmcnt(4)
	v_mfma_f32_16x16x32_bf16 v[126:129], v[122:125], v[184:187], v[126:129]
	s_waitcnt lgkmcnt(2)
	v_mfma_f32_16x16x32_bf16 v[152:155], v[216:219], v[184:187], v[152:155]
	s_waitcnt lgkmcnt(0)
	v_mfma_f32_16x16x32_bf16 v[164:167], v[220:223], v[184:187], v[164:167]
	v_mfma_f32_16x16x32_bf16 v[168:171], v[110:113], v[204:207], v[168:171]
	v_mfma_f32_16x16x32_bf16 v[172:175], v[122:125], v[204:207], v[172:175]
	v_mfma_f32_16x16x32_bf16 v[176:179], v[216:219], v[204:207], v[176:179]
	v_mfma_f32_16x16x32_bf16 v[114:117], v[220:223], v[204:207], v[114:117]
	v_mfma_f32_16x16x32_bf16 v[184:187], v[110:113], v[212:215], v[188:191]
	v_mfma_f32_16x16x32_bf16 v[188:191], v[122:125], v[212:215], v[192:195]
	v_mfma_f32_16x16x32_bf16 v[192:195], v[216:219], v[212:215], v[196:199]
	s_nop 2
	ds_read_b128 v[196:199], v62 offset:53056
	ds_read_b128 v[204:207], v62 offset:55360
	s_waitcnt vmcnt(8)
	ds_write_b128 v86, v[40:43]
	s_waitcnt vmcnt(7)
	ds_write_b128 v86, v[44:47] offset:9216
	v_mfma_f32_16x16x32_bf16 v[32:35], v[220:223], v[212:215], v[32:35]
	s_waitcnt lgkmcnt(3)
	v_mfma_f32_16x16x32_bf16 v[40:43], v[110:113], v[196:199], v[8:11]
	v_mfma_f32_16x16x32_bf16 v[44:47], v[122:125], v[196:199], v[12:15]
	v_mfma_f32_16x16x32_bf16 v[36:39], v[216:219], v[196:199], v[36:39]
	v_mfma_f32_16x16x32_bf16 v[180:183], v[220:223], v[196:199], v[180:183]
	s_waitcnt lgkmcnt(2)
	v_mfma_f32_16x16x32_bf16 v[102:105], v[110:113], v[204:207], v[102:105]
	v_mfma_f32_16x16x32_bf16 v[106:109], v[122:125], v[204:207], v[106:109]
	global_load_dwordx4 v[110:113], v[52:53], off offset:384
	s_nop 0
	global_load_dwordx4 v[52:55], v[54:55], off offset:384
	s_nop 0
	global_load_dwordx4 v[122:125], v[56:57], off offset:384
	s_nop 0
	global_load_dwordx4 v[56:59], v[58:59], off offset:384
	s_nop 0
	global_load_dwordx4 v[196:199], v[60:61], off offset:384
	s_waitcnt vmcnt(11)
	ds_write_b128 v86, v[48:51] offset:18432
	s_waitcnt vmcnt(10)
	ds_write_b128 v86, v[200:203] offset:27648
	s_waitcnt vmcnt(9)
	ds_write_b128 v86, v[208:211] offset:36864
	v_mfma_f32_16x16x32_bf16 v[48:51], v[220:223], v[204:207], v[0:3]
	v_mfma_f32_16x16x32_bf16 v[212:215], v[216:219], v[204:207], v[4:7]
	s_waitcnt lgkmcnt(0)
	s_barrier
	ds_read_b64_tr_b16 v[200:201], v81
	ds_read_b64_tr_b16 v[202:203], v82
	ds_read_b64_tr_b16 v[204:205], v83
	ds_read_b64_tr_b16 v[206:207], v84
	ds_read_b128 v[0:3], v62
	ds_read_b64_tr_b16 v[208:209], v79
	ds_read_b64_tr_b16 v[210:211], v80
	ds_read_b128 v[4:7], v62 offset:2304
	s_cmpk_lt_i32 s24, 0x100
	s_cselect_b32 s8, s24, 0
	s_waitcnt lgkmcnt(3)
	v_mfma_f32_16x16x32_bf16 v[80:83], v[200:203], v[0:3], v[118:121]
	s_nop 2
	ds_read_b64_tr_b16 v[118:119], v100
	ds_read_b64_tr_b16 v[120:121], v101
	s_cselect_b32 s10, s51, s57
	s_cselect_b32 s11, s50, s56
	s_ashr_i32 s9, s8, 31
	s_lshl_b64 s[8:9], s[8:9], 20
	s_add_u32 s8, s11, s8
	s_addc_u32 s9, s10, s9
	s_lshl_b32 s10, s25, 7
	s_ashr_i32 s11, s10, 31
	v_mfma_f32_16x16x32_bf16 v[126:129], v[204:207], v[0:3], v[126:129]
	s_lshl_b64 s[10:11], s[10:11], 2
	ds_read_b128 v[216:219], v62 offset:4608
	s_waitcnt vmcnt(8)
	v_cvt_pk_bf16_f32 v28, v28, v29
	s_waitcnt lgkmcnt(4)
	v_mfma_f32_16x16x32_bf16 v[152:155], v[208:211], v[0:3], v[152:155]
	v_cvt_pk_bf16_f32 v29, v30, v31
	s_waitcnt vmcnt(7)
	v_cvt_pk_bf16_f32 v24, v24, v25
	v_cvt_pk_bf16_f32 v25, v26, v27
	s_waitcnt lgkmcnt(1)
	v_mfma_f32_16x16x32_bf16 v[164:167], v[118:121], v[0:3], v[164:167]
	v_lshl_add_u64 v[0:1], s[8:9], 0, v[136:137]
	v_lshl_add_u64 v[0:1], v[0:1], 0, s[10:11]
	v_lshl_add_u64 v[0:1], v[0:1], 0, v[132:133]
	v_lshl_add_u64 v[0:1], v[0:1], 0, v[148:149]
	v_lshl_add_u64 v[8:9], v[0:1], 0, v[150:151]
	v_add_co_u32_e32 v0, vcc, s16, v8
	v_mfma_f32_16x16x32_bf16 v[168:171], v[200:203], v[4:7], v[168:171]
	s_nop 0
	v_addc_co_u32_e32 v1, vcc, 0, v9, vcc
	v_add_co_u32_e32 v10, vcc, s17, v8
	v_mfma_f32_16x16x32_bf16 v[172:175], v[204:207], v[4:7], v[172:175]
	s_nop 0
	v_addc_co_u32_e32 v11, vcc, 0, v9, vcc
	v_mfma_f32_16x16x32_bf16 v[176:179], v[208:211], v[4:7], v[176:179]
	v_mfma_f32_16x16x32_bf16 v[114:117], v[118:121], v[4:7], v[114:117]
	global_load_dwordx4 v[4:7], v[8:9], off
	s_nop 0
	global_load_dwordx4 v[0:3], v[0:1], off
	v_add_co_u32_e32 v8, vcc, s18, v8
	ds_read_b128 v[220:223], v62 offset:6912
	s_nop 0
	v_addc_co_u32_e32 v9, vcc, 0, v9, vcc
	global_load_dwordx4 v[12:15], v[10:11], off
	s_nop 0
	global_load_dwordx4 v[8:11], v[8:9], off
	ds_read_b128 v[224:227], v62 offset:9216
	s_waitcnt lgkmcnt(2)
	v_mfma_f32_16x16x32_bf16 v[32:35], v[118:121], v[216:219], v[32:35]
	ds_write_b64 v99, v[28:29]
	ds_write_b64 v98, v[24:25]
	v_mfma_f32_16x16x32_bf16 v[184:187], v[200:203], v[216:219], v[184:187]
	v_mfma_f32_16x16x32_bf16 v[188:191], v[204:207], v[216:219], v[188:191]
	v_mfma_f32_16x16x32_bf16 v[192:195], v[208:211], v[216:219], v[192:195]
	s_waitcnt lgkmcnt(3)
	v_mfma_f32_16x16x32_bf16 v[28:31], v[204:207], v[220:223], v[44:47]
	s_waitcnt vmcnt(9)
	v_cvt_pk_bf16_f32 v16, v16, v17
	v_cvt_pk_bf16_f32 v17, v18, v19
	v_cvt_pk_bf16_f32 v60, v20, v21
	s_waitcnt lgkmcnt(2)
	v_mfma_f32_16x16x32_bf16 v[44:47], v[200:203], v[224:227], v[102:105]
	ds_read_b128 v[98:101], v62 offset:64
	s_nop 1
	ds_read_b128 v[102:105], v62 offset:2368
	v_cvt_pk_bf16_f32 v61, v22, v23
	v_mfma_f32_16x16x32_bf16 v[24:27], v[200:203], v[220:223], v[40:43]
	v_mfma_f32_16x16x32_bf16 v[36:39], v[208:211], v[220:223], v[36:39]
	v_mfma_f32_16x16x32_bf16 v[40:43], v[118:121], v[220:223], v[180:183]
	v_mfma_f32_16x16x32_bf16 v[106:109], v[204:207], v[224:227], v[106:109]
	s_nop 1
	ds_read_b128 v[180:183], v62 offset:4672
	ds_write_b64 v92, v[16:17]
	ds_write_b64 v95, v[60:61]
	v_mfma_f32_16x16x32_bf16 v[20:23], v[208:211], v[224:227], v[212:215]
	v_mfma_f32_16x16x32_bf16 v[16:19], v[118:121], v[224:227], v[48:51]
	s_nop 2
	ds_read_b64_tr_b16 v[48:49], v91
	ds_read_b64_tr_b16 v[50:51], v93
	ds_read_b64_tr_b16 v[118:119], v89
	ds_read_b64_tr_b16 v[120:121], v90
	ds_read_b64_tr_b16 v[90:91], v85
	ds_read_b64_tr_b16 v[92:93], v94
	ds_read_b64_tr_b16 v[94:95], v96
	ds_read_b64_tr_b16 v[96:97], v97
	s_waitcnt lgkmcnt(6)
	v_mfma_f32_16x16x32_bf16 v[80:83], v[48:51], v[98:101], v[80:83]
	s_waitcnt lgkmcnt(4)
	v_mfma_f32_16x16x32_bf16 v[126:129], v[118:121], v[98:101], v[126:129]
	s_waitcnt lgkmcnt(2)
	v_mfma_f32_16x16x32_bf16 v[152:155], v[90:93], v[98:101], v[152:155]
	s_waitcnt lgkmcnt(0)
	v_mfma_f32_16x16x32_bf16 v[98:101], v[94:97], v[98:101], v[164:167]
	v_mfma_f32_16x16x32_bf16 v[164:167], v[48:51], v[102:105], v[168:171]
	v_mfma_f32_16x16x32_bf16 v[168:171], v[118:121], v[102:105], v[172:175]
	v_mfma_f32_16x16x32_bf16 v[172:175], v[90:93], v[102:105], v[176:179]
	v_mfma_f32_16x16x32_bf16 v[102:105], v[94:97], v[102:105], v[114:117]
	v_mfma_f32_16x16x32_bf16 v[114:117], v[48:51], v[180:183], v[184:187]
	v_mfma_f32_16x16x32_bf16 v[176:179], v[118:121], v[180:183], v[188:191]
	v_mfma_f32_16x16x32_bf16 v[184:187], v[90:93], v[180:183], v[192:195]
	s_nop 1
	ds_read_b128 v[188:191], v62 offset:6976
	ds_read_b128 v[192:195], v62 offset:9280
	s_waitcnt vmcnt(8)
	ds_write_b128 v86, v[110:113] offset:46080
	s_waitcnt vmcnt(7)
	ds_write_b128 v86, v[52:55] offset:55296
	v_mfma_f32_16x16x32_bf16 v[52:55], v[94:97], v[180:183], v[32:35]
	s_waitcnt lgkmcnt(3)
	v_mfma_f32_16x16x32_bf16 v[110:113], v[48:51], v[188:191], v[24:27]
	s_waitcnt vmcnt(6)
	ds_write_b128 v86, v[122:125] offset:64512
	s_waitcnt vmcnt(5)
	ds_write_b128 v87, v[56:59]
	s_waitcnt vmcnt(4)
	ds_write_b128 v88, v[196:199]
	v_mfma_f32_16x16x32_bf16 v[180:183], v[118:121], v[188:191], v[28:31]
	v_mfma_f32_16x16x32_bf16 v[200:203], v[90:93], v[188:191], v[36:39]
	v_mfma_f32_16x16x32_bf16 v[188:191], v[94:97], v[188:191], v[40:43]
	s_waitcnt lgkmcnt(5)
	v_mfma_f32_16x16x32_bf16 v[94:97], v[94:97], v[192:195], v[16:19]
	s_nop 2
	v_sub_u32_e32 v16, v163, v143
	v_xad_u32 v18, s26, -1, v16
	v_add_u32_e32 v17, s26, v162
	v_min_i32_e32 v16, 0, v18
	v_add_u32_e32 v19, v17, v143
	v_add_u32_e32 v16, v16, v19
	v_ashrrev_i32_e32 v17, 31, v16
	v_lshlrev_b64 v[16:17], 9, v[16:17]
	v_lshl_add_u64 v[16:17], v[134:135], 0, v[16:17]
	global_load_dwordx4 v[32:35], v[16:17], off
	v_min_i32_e32 v16, 64, v18
	v_add_u32_e32 v16, v16, v19
	v_ashrrev_i32_e32 v17, 31, v16
	v_lshlrev_b64 v[16:17], 9, v[16:17]
	v_lshl_add_u64 v[16:17], v[134:135], 0, v[16:17]
	global_load_dwordx4 v[36:39], v[16:17], off
	v_min_i32_e32 v16, 0x80, v18
	v_add_u32_e32 v16, v16, v19
	v_ashrrev_i32_e32 v17, 31, v16
	v_lshlrev_b64 v[16:17], 9, v[16:17]
	v_lshl_add_u64 v[16:17], v[134:135], 0, v[16:17]
	global_load_dwordx4 v[40:43], v[16:17], off
	v_min_i32_e32 v16, 0xc0, v18
	v_add_u32_e32 v16, v16, v19
	v_ashrrev_i32_e32 v17, 31, v16
	v_lshlrev_b64 v[16:17], 9, v[16:17]
	v_lshl_add_u64 v[16:17], v[134:135], 0, v[16:17]
	v_mfma_f32_16x16x32_bf16 v[204:207], v[48:51], v[192:195], v[44:47]
	s_nop 2
	global_load_dwordx4 v[44:47], v[16:17], off
	v_min_i32_e32 v16, 0x100, v18
	v_add_u32_e32 v16, v16, v19
	v_ashrrev_i32_e32 v17, 31, v16
	v_lshlrev_b64 v[16:17], 9, v[16:17]
	v_lshl_add_u64 v[16:17], v[134:135], 0, v[16:17]
	global_load_dwordx4 v[48:51], v[16:17], off
	v_mfma_f32_16x16x32_bf16 v[106:109], v[118:121], v[192:195], v[106:109]
	v_mfma_f32_16x16x32_bf16 v[90:93], v[90:93], v[192:195], v[20:23]
	s_waitcnt lgkmcnt(0)
	s_barrier
	ds_read_b64_tr_b16 v[56:57], v77
	ds_read_b64_tr_b16 v[58:59], v78
	ds_read_b128 v[16:19], v62 offset:46080
	ds_read_b64_tr_b16 v[84:85], v74
	ds_read_b64_tr_b16 v[86:87], v75
	ds_read_b64_tr_b16 v[74:75], v76
	ds_read_b128 v[20:23], v62 offset:48384
	ds_read_b128 v[118:121], v62 offset:55296
	ds_read_b64_tr_b16 v[76:77], v73
	s_waitcnt lgkmcnt(4)
	v_mfma_f32_16x16x32_bf16 v[122:125], v[84:87], v[16:19], v[126:129]
	s_nop 2
	ds_read_b64_tr_b16 v[126:127], v71
	ds_read_b64_tr_b16 v[128:129], v72
	ds_read_b128 v[192:195], v62 offset:50688
	v_mfma_f32_16x16x32_bf16 v[78:81], v[56:59], v[16:19], v[80:83]
	s_waitcnt lgkmcnt(3)
	v_mfma_f32_16x16x32_bf16 v[152:155], v[74:77], v[16:19], v[152:155]
	s_waitcnt lgkmcnt(1)
	v_mfma_f32_16x16x32_bf16 v[98:101], v[126:129], v[16:19], v[98:101]
	v_lshl_add_u64 v[16:17], s[8:9], 0, v[138:139]
	v_lshl_add_u64 v[16:17], v[16:17], 0, s[10:11]
	v_lshl_add_u64 v[16:17], v[16:17], 0, v[132:133]
	v_lshl_add_u64 v[16:17], v[16:17], 0, v[148:149]
	v_lshl_add_u64 v[16:17], v[16:17], 0, v[150:151]
	v_add_co_u32_e32 v18, vcc, s16, v16
	v_mfma_f32_16x16x32_bf16 v[164:167], v[56:59], v[20:23], v[164:167]
	s_nop 0
	v_addc_co_u32_e32 v19, vcc, 0, v17, vcc
	global_load_dwordx4 v[28:31], v[16:17], off
	global_load_dwordx4 v[24:27], v[18:19], off
	v_add_co_u32_e32 v18, vcc, s17, v16
	v_mfma_f32_16x16x32_bf16 v[168:171], v[84:87], v[20:23], v[168:171]
	s_nop 0
	v_addc_co_u32_e32 v19, vcc, 0, v17, vcc
	v_add_co_u32_e32 v16, vcc, s18, v16
	v_mfma_f32_16x16x32_bf16 v[172:175], v[74:77], v[20:23], v[172:175]
	s_nop 0
	v_addc_co_u32_e32 v17, vcc, 0, v17, vcc
	v_mfma_f32_16x16x32_bf16 v[196:199], v[126:129], v[20:23], v[102:105]
	s_nop 2
	ds_read_b128 v[102:105], v62 offset:52992
	global_load_dwordx4 v[20:23], v[18:19], off
	s_nop 0
	global_load_dwordx4 v[16:19], v[16:17], off
	s_waitcnt lgkmcnt(1)
	v_mfma_f32_16x16x32_bf16 v[52:55], v[126:129], v[192:195], v[52:55]
	v_mfma_f32_16x16x32_bf16 v[208:211], v[56:59], v[192:195], v[114:117]
	v_mfma_f32_16x16x32_bf16 v[176:179], v[84:87], v[192:195], v[176:179]
	v_mfma_f32_16x16x32_bf16 v[184:187], v[74:77], v[192:195], v[184:187]
	s_waitcnt lgkmcnt(0)
	v_mfma_f32_16x16x32_bf16 v[192:195], v[56:59], v[102:105], v[110:113]
	v_mfma_f32_16x16x32_bf16 v[180:183], v[84:87], v[102:105], v[180:183]
	v_mfma_f32_16x16x32_bf16 v[200:203], v[74:77], v[102:105], v[200:203]
	v_mfma_f32_16x16x32_bf16 v[56:59], v[56:59], v[118:121], v[204:207]
	v_mfma_f32_16x16x32_bf16 v[204:207], v[84:87], v[118:121], v[106:109]
	v_mfma_f32_16x16x32_bf16 v[212:215], v[74:77], v[118:121], v[90:93]
	ds_read_b128 v[72:75], v62 offset:46144
	ds_read_b128 v[82:85], v62 offset:48448
	s_nop 0
	ds_read_b128 v[88:91], v62 offset:50752
	v_mfma_f32_16x16x32_bf16 v[188:191], v[126:129], v[102:105], v[188:191]
	v_mfma_f32_16x16x32_bf16 v[216:219], v[126:129], v[118:121], v[94:97]
	ds_read_b64_tr_b16 v[220:221], v68
	ds_read_b64_tr_b16 v[222:223], v70
	ds_read_b64_tr_b16 v[224:225], v67
	ds_read_b64_tr_b16 v[226:227], v69
	ds_read_b64_tr_b16 v[228:229], v65
	ds_read_b64_tr_b16 v[230:231], v66
	ds_read_b64_tr_b16 v[232:233], v63
	ds_read_b64_tr_b16 v[234:235], v64
	s_waitcnt lgkmcnt(6)
	v_mfma_f32_16x16x32_bf16 v[116:119], v[220:223], v[72:75], v[78:81]
	s_waitcnt lgkmcnt(4)
	v_mfma_f32_16x16x32_bf16 v[128:131], v[224:227], v[72:75], v[122:125]
	s_waitcnt lgkmcnt(2)
	v_mfma_f32_16x16x32_bf16 v[120:123], v[228:231], v[72:75], v[152:155]
	ds_read_b128 v[64:67], v62 offset:53056
	s_nop 1
	ds_read_b128 v[152:155], v62 offset:55360
	s_waitcnt lgkmcnt(2)
	v_mfma_f32_16x16x32_bf16 v[124:127], v[232:235], v[72:75], v[98:101]
	v_mfma_f32_16x16x32_bf16 v[112:115], v[220:223], v[82:85], v[164:167]
	v_mfma_f32_16x16x32_bf16 v[108:111], v[224:227], v[82:85], v[168:171]
	v_mfma_f32_16x16x32_bf16 v[104:107], v[228:231], v[82:85], v[172:175]
	v_mfma_f32_16x16x32_bf16 v[100:103], v[232:235], v[82:85], v[196:199]
	v_mfma_f32_16x16x32_bf16 v[96:99], v[220:223], v[88:91], v[208:211]
	v_mfma_f32_16x16x32_bf16 v[92:95], v[224:227], v[88:91], v[176:179]
	v_mfma_f32_16x16x32_bf16 v[84:87], v[228:231], v[88:91], v[184:187]
	v_mfma_f32_16x16x32_bf16 v[88:91], v[232:235], v[88:91], v[52:55]
	s_waitcnt lgkmcnt(1)
	v_mfma_f32_16x16x32_bf16 v[80:83], v[220:223], v[64:67], v[192:195]
	v_mfma_f32_16x16x32_bf16 v[76:79], v[224:227], v[64:67], v[180:183]
	v_mfma_f32_16x16x32_bf16 v[72:75], v[228:231], v[64:67], v[200:203]
	v_mfma_f32_16x16x32_bf16 v[68:71], v[232:235], v[64:67], v[188:191]
	s_waitcnt lgkmcnt(0)
	v_mfma_f32_16x16x32_bf16 v[64:67], v[220:223], v[152:155], v[56:59]
	v_mfma_f32_16x16x32_bf16 v[60:63], v[224:227], v[152:155], v[204:207]
	v_mfma_f32_16x16x32_bf16 v[56:59], v[228:231], v[152:155], v[212:215]
	v_mfma_f32_16x16x32_bf16 v[52:55], v[232:235], v[152:155], v[216:219]
	v_add_u32_e32 v149, s14, v157
	v_cmp_lt_i32_e32 vcc, v149, v156
	v_lshlrev_b32_e32 v154, 1, v140
	v_lshlrev_b32_e32 v152, 1, v142
	v_and_b32_e32 v248, 16, v142
	v_sub_u32_e32 v152, v152, v248
	s_and_saveexec_b64 s[8:9], vcc
	s_cbranch_execz .LBB0_908
	v_add_u32_e32 v164, v141, v149
	v_ashrrev_i32_e32 v165, 31, v164
	v_readlane_b32 s10, v254, 3
	v_lshlrev_b64 v[164:165], 11, v[164:165]
	v_readlane_b32 s11, v254, 4
	v_mov_b32_e32 v155, v133
	v_mov_b32_e32 v153, v133
	v_lshl_add_u64 v[164:165], s[10:11], 0, v[164:165]
	v_lshl_add_u64 v[164:165], s[6:7], 1, v[164:165]
	v_lshl_add_u64 v[164:165], v[164:165], 0, v[154:155]
	v_lshl_add_u64 v[164:165], v[164:165], 0, v[152:153]
	v_cvt_pk_bf16_f32 v116, v116, v117
	v_cvt_pk_bf16_f32 v117, v118, v119
	v_cvt_pk_bf16_f32 v118, v128, v129
	v_cvt_pk_bf16_f32 v119, v130, v131
	v_mov_b32_e32 v244, v116
	v_mov_b32_e32 v245, v117
	v_mov_b32_e32 v246, v118
	v_mov_b32_e32 v247, v119
	s_nop 1
	v_cvt_pk_bf16_f32 v116, v120, v121
	v_cvt_pk_bf16_f32 v117, v122, v123
	v_cvt_pk_bf16_f32 v118, v124, v125
	v_cvt_pk_bf16_f32 v119, v126, v127
	s_nop 1
	v_permlane16_swap_b32 v244, v116
	v_permlane16_swap_b32 v245, v117
	v_permlane16_swap_b32 v246, v118
	v_permlane16_swap_b32 v247, v119
	global_store_dwordx4 v[164:165], v[244:247], off
	global_store_dwordx4 v[164:165], v[116:119], off offset:32
.LBB0_908:
	s_or_b64 exec, exec, s[8:9]
	s_nop 0
	v_add_u32_e32 v116, s14, v158
	v_cmp_lt_i32_e32 vcc, v116, v156
	s_and_saveexec_b64 s[8:9], vcc
	s_cbranch_execz .LBB0_910
	v_add_u32_e32 v116, v141, v116
	v_ashrrev_i32_e32 v117, 31, v116
	v_readlane_b32 s10, v254, 3
	v_lshlrev_b64 v[116:117], 11, v[116:117]
	v_readlane_b32 s11, v254, 4
	v_mov_b32_e32 v155, v133
	v_mov_b32_e32 v153, v133
	v_lshl_add_u64 v[116:117], s[10:11], 0, v[116:117]
	v_lshl_add_u64 v[116:117], s[6:7], 1, v[116:117]
	v_lshl_add_u64 v[116:117], v[116:117], 0, v[154:155]
	v_lshl_add_u64 v[116:117], v[116:117], 0, v[152:153]
	v_cvt_pk_bf16_f32 v112, v112, v113
	v_cvt_pk_bf16_f32 v113, v114, v115
	v_cvt_pk_bf16_f32 v114, v108, v109
	v_cvt_pk_bf16_f32 v115, v110, v111
	v_cvt_pk_bf16_f32 v104, v104, v105
	v_cvt_pk_bf16_f32 v105, v106, v107
	v_cvt_pk_bf16_f32 v106, v100, v101
	v_cvt_pk_bf16_f32 v107, v102, v103
	s_nop 1
	v_permlane16_swap_b32 v112, v104
	v_permlane16_swap_b32 v113, v105
	v_permlane16_swap_b32 v114, v106
	v_permlane16_swap_b32 v115, v107
	global_store_dwordx4 v[116:117], v[112:115], off
	global_store_dwordx4 v[116:117], v[104:107], off offset:32
.LBB0_910:
	s_or_b64 exec, exec, s[8:9]
	v_add_u32_e32 v100, s14, v159
	v_cmp_lt_i32_e32 vcc, v100, v156
	s_and_saveexec_b64 s[8:9], vcc
	s_cbranch_execz .LBB0_912
	v_add_u32_e32 v100, v141, v100
	v_ashrrev_i32_e32 v101, 31, v100
	v_readlane_b32 s10, v254, 3
	v_lshlrev_b64 v[100:101], 11, v[100:101]
	v_readlane_b32 s11, v254, 4
	v_mov_b32_e32 v155, v133
	v_mov_b32_e32 v153, v133
	v_lshl_add_u64 v[100:101], s[10:11], 0, v[100:101]
	v_lshl_add_u64 v[100:101], s[6:7], 1, v[100:101]
	v_lshl_add_u64 v[100:101], v[100:101], 0, v[154:155]
	v_lshl_add_u64 v[100:101], v[100:101], 0, v[152:153]
	v_cvt_pk_bf16_f32 v96, v96, v97
	v_cvt_pk_bf16_f32 v97, v98, v99
	v_cvt_pk_bf16_f32 v98, v92, v93
	v_cvt_pk_bf16_f32 v99, v94, v95
	v_cvt_pk_bf16_f32 v84, v84, v85
	v_cvt_pk_bf16_f32 v85, v86, v87
	v_cvt_pk_bf16_f32 v86, v88, v89
	v_cvt_pk_bf16_f32 v87, v90, v91
	s_nop 1
	v_permlane16_swap_b32 v96, v84
	v_permlane16_swap_b32 v97, v85
	v_permlane16_swap_b32 v98, v86
	v_permlane16_swap_b32 v99, v87
	global_store_dwordx4 v[100:101], v[96:99], off
	global_store_dwordx4 v[100:101], v[84:87], off offset:32
.LBB0_912:
	s_or_b64 exec, exec, s[8:9]
	s_nop 0
	v_add_u32_e32 v84, s14, v160
	v_cmp_lt_i32_e32 vcc, v84, v156
	s_and_saveexec_b64 s[8:9], vcc
	s_cbranch_execz .LBB0_914
	v_add_u32_e32 v84, v141, v84
	v_ashrrev_i32_e32 v85, 31, v84
	v_readlane_b32 s10, v254, 3
	v_lshlrev_b64 v[84:85], 11, v[84:85]
	v_readlane_b32 s11, v254, 4
	v_mov_b32_e32 v155, v133
	v_mov_b32_e32 v153, v133
	v_lshl_add_u64 v[84:85], s[10:11], 0, v[84:85]
	v_lshl_add_u64 v[84:85], s[6:7], 1, v[84:85]
	v_lshl_add_u64 v[84:85], v[84:85], 0, v[154:155]
	v_lshl_add_u64 v[84:85], v[84:85], 0, v[152:153]
	v_cvt_pk_bf16_f32 v80, v80, v81
	v_cvt_pk_bf16_f32 v81, v82, v83
	v_cvt_pk_bf16_f32 v82, v76, v77
	v_cvt_pk_bf16_f32 v83, v78, v79
	v_cvt_pk_bf16_f32 v72, v72, v73
	v_cvt_pk_bf16_f32 v73, v74, v75
	v_cvt_pk_bf16_f32 v74, v68, v69
	v_cvt_pk_bf16_f32 v75, v70, v71
	s_nop 1
	v_permlane16_swap_b32 v80, v72
	v_permlane16_swap_b32 v81, v73
	v_permlane16_swap_b32 v82, v74
	v_permlane16_swap_b32 v83, v75
	global_store_dwordx4 v[84:85], v[80:83], off
	global_store_dwordx4 v[84:85], v[72:75], off offset:32

.LBB0_916:
	v_add_u32_e32 v68, v141, v68
	v_ashrrev_i32_e32 v69, 31, v68
	v_readlane_b32 s10, v254, 3
	v_lshlrev_b64 v[68:69], 11, v[68:69]
	v_readlane_b32 s11, v254, 4
	v_mov_b32_e32 v155, v133
	v_mov_b32_e32 v153, v133
	v_lshl_add_u64 v[68:69], s[10:11], 0, v[68:69]
	v_lshl_add_u64 v[68:69], s[6:7], 1, v[68:69]
	v_lshl_add_u64 v[68:69], v[68:69], 0, v[154:155]
	v_lshl_add_u64 v[68:69], v[68:69], 0, v[152:153]
	v_cvt_pk_bf16_f32 v64, v64, v65
	v_cvt_pk_bf16_f32 v65, v66, v67
	v_cvt_pk_bf16_f32 v66, v60, v61
	v_cvt_pk_bf16_f32 v67, v62, v63
	v_cvt_pk_bf16_f32 v56, v56, v57
	v_cvt_pk_bf16_f32 v57, v58, v59
	v_cvt_pk_bf16_f32 v58, v52, v53
	v_cvt_pk_bf16_f32 v59, v54, v55
	s_nop 1
	v_permlane16_swap_b32 v64, v56
	v_permlane16_swap_b32 v65, v57
	v_permlane16_swap_b32 v66, v58
	v_permlane16_swap_b32 v67, v59
	global_store_dwordx4 v[68:69], v[64:67], off
	global_store_dwordx4 v[68:69], v[56:59], off offset:32
	s_or_b64 exec, exec, s[8:9]
	s_andn2_b64 vcc, exec, s[4:5]
	s_cbranch_vccnz .LBB0_901

.LBB0_2485:
	s_getreg_b32 s6, hwreg(HW_REG_HW_ID, 0, 6)
	s_lshl_b32 s6, s6, 2
	s_add_i32 s6, s6, 0x27000
	v_mov_b32_e32 v52, s6
	ds_read_b32 v52, v52
	v_mov_b32_e32 v53, 0
	s_waitcnt vmcnt(7)
	v_cvt_pk_bf16_f32 v20, v20, v21
	v_mbcnt_lo_u32_b32 v53, -1, v53
	v_mbcnt_hi_u32_b32 v53, -1, v53
	s_waitcnt lgkmcnt(0)
	v_readfirstlane_b32 s6, v52
	v_cvt_pk_bf16_f32 v21, v22, v23
	s_waitcnt vmcnt(6)
	v_cvt_pk_bf16_f32 v16, v16, v17
	v_lshl_or_b32 v62, s6, 6, v53
	v_cvt_pk_bf16_f32 v17, v18, v19
	v_lshrrev_b32_e32 v53, 3, v62
	v_lshlrev_b32_e32 v54, 4, v62
	v_and_b32_e32 v68, 0x70, v54
	v_mul_lo_u32 v69, v53, s22
	v_ashrrev_i32_e32 v52, 5, v62
	v_add3_u32 v53, 0, v68, v69
	ds_write_b128 v53, v[36:39]
	ds_write_b128 v53, v[32:35] offset:9216
	ds_write_b128 v53, v[44:47] offset:18432
	s_waitcnt vmcnt(5)
	ds_write_b128 v53, v[40:43] offset:27648
	s_waitcnt vmcnt(4)
	ds_write_b128 v53, v[48:51] offset:36864
	v_lshrrev_b32_e32 v34, 1, v52
	v_bfe_u32 v32, v62, 2, 3
	v_and_b32_e32 v33, 3, v52
	v_and_b32_e32 v34, 4, v34
	v_bitop3_b32 v32, v34, v32, v33 bitop3:0x36
	v_lshlrev_b32_e32 v33, 2, v62
	v_and_b32_e32 v36, 12, v33
	v_lshlrev_b32_e32 v37, 1, v36
	v_lshl_or_b32 v70, v32, 5, v37
	v_lshlrev_b32_e32 v172, 8, v52
	v_add3_u32 v22, s23, v70, v172
	ds_write2st64_b64 v22, v[20:21], v[16:17] offset1:8
	s_waitcnt vmcnt(5)
	v_cvt_pk_bf16_f32 v16, v28, v29
	v_cvt_pk_bf16_f32 v17, v30, v31
	s_waitcnt vmcnt(4)
	v_cvt_pk_bf16_f32 v18, v24, v25
	v_cvt_pk_bf16_f32 v19, v26, v27
	ds_write2st64_b64 v22, v[16:17], v[18:19] offset0:16 offset1:24
	v_sub_u32_e32 v16, v156, v143
	v_xad_u32 v32, s14, -1, v16
	v_add_u32_e32 v17, s14, v141
	v_lshrrev_b32_e32 v39, 2, v62
	v_bfe_u32 v65, v62, 2, 2
	v_min_i32_e32 v16, 0, v32
	v_add_u32_e32 v33, v17, v143
	v_and_b32_e32 v39, 4, v39
	v_bfe_u32 v66, v62, 6, 1
	v_add_u32_e32 v16, v16, v33
	v_or_b32_e32 v40, v39, v65
	v_ashrrev_i32_e32 v17, 31, v16
	v_lshlrev_b32_e32 v41, 6, v66
	v_lshlrev_b32_e32 v40, 4, v40
	v_lshlrev_b64 v[16:17], 9, v[16:17]
	v_lshrrev_b32_e32 v38, 1, v62
	v_xor_b32_e32 v40, v40, v41
	s_cmpk_lt_i32 s13, 0x100
	v_readlane_b32 s36, v253, 4
	v_lshl_add_u64 v[52:53], v[134:135], 0, v[16:17]
	v_min_i32_e32 v16, 64, v32
	v_and_b32_e32 v67, 24, v38
	v_or_b32_e32 v36, v40, v36
	s_cselect_b32 s6, s13, 1
	v_readlane_b32 s48, v253, 16
	v_readlane_b32 s49, v253, 17
	v_add_u32_e32 v16, v16, v33
	v_or_b32_e32 v38, v67, v65
	v_lshlrev_b32_e32 v188, 1, v36
	v_lshlrev_b32_e32 v36, 2, v66
	s_cselect_b32 s9, s17, s49
	s_cselect_b32 s8, s16, s48
	s_ashr_i32 s7, s6, 31
	v_ashrrev_i32_e32 v17, 31, v16
	v_lshlrev_b32_e32 v71, 8, v38
	v_or_b32_e32 v38, 1, v36
	s_lshl_b64 s[6:7], s[6:7], 20
	v_lshlrev_b64 v[16:17], 9, v[16:17]
	v_bitop3_b32 v38, v39, v38, v65 bitop3:0x36
	s_add_u32 s8, s8, s6
	v_lshl_add_u64 v[54:55], v[134:135], 0, v[16:17]
	v_min_i32_e32 v16, 0x80, v32
	v_lshl_or_b32 v192, v38, 5, v37
	v_or_b32_e32 v38, 2, v36
	v_or_b32_e32 v36, 3, v36
	s_addc_u32 s9, s9, s7
	s_lshl_b32 s6, s15, 7
	v_add_u32_e32 v16, v16, v33
	v_bitop3_b32 v38, v39, v38, v65 bitop3:0x36
	v_bitop3_b32 v36, v39, v36, v65 bitop3:0x36
	s_ashr_i32 s7, s6, 31
	v_ashrrev_i32_e32 v17, 31, v16
	v_lshl_or_b32 v193, v38, 5, v37
	v_lshl_or_b32 v196, v36, 5, v37
	v_lshl_add_u64 v[36:37], s[8:9], 0, v[144:145]
	s_lshl_b64 s[10:11], s[6:7], 2
	v_lshlrev_b64 v[16:17], 9, v[16:17]
	v_lshl_add_u64 v[36:37], v[36:37], 0, s[10:11]
	v_lshl_add_u64 v[56:57], v[134:135], 0, v[16:17]
	v_min_i32_e32 v16, 0xc0, v32
	v_min_i32_e32 v32, 0x100, v32
	v_lshl_add_u64 v[36:37], v[36:37], 0, v[132:133]
	v_mov_b32_e32 v149, v133
	v_add_u32_e32 v32, v32, v33
	v_lshl_add_u64 v[36:37], v[36:37], 0, v[148:149]
	v_mov_b32_e32 v151, v133
	v_add_u32_e32 v16, v16, v33
	v_ashrrev_i32_e32 v33, 31, v32
	v_lshl_add_u64 v[36:37], v[36:37], 0, v[150:151]
	v_ashrrev_i32_e32 v17, 31, v16
	v_lshlrev_b64 v[32:33], 9, v[32:33]
	v_add_co_u32_e32 v38, vcc, s18, v36
	v_lshlrev_b64 v[16:17], 9, v[16:17]
	v_lshl_add_u64 v[60:61], v[134:135], 0, v[32:33]
	v_addc_co_u32_e32 v39, vcc, 0, v37, vcc
	global_load_dwordx4 v[24:27], v[52:53], off offset:128
	global_load_dwordx4 v[28:31], v[54:55], off offset:128
	v_lshl_add_u64 v[58:59], v[134:135], 0, v[16:17]
	global_load_dwordx4 v[16:19], v[56:57], off offset:128
	global_load_dwordx4 v[20:23], v[58:59], off offset:128
	global_load_dwordx4 v[32:35], v[60:61], off offset:128
	s_waitcnt lgkmcnt(0)
	s_barrier
	global_load_dwordx4 v[48:51], v[36:37], off
	global_load_dwordx4 v[44:47], v[38:39], off
	v_add_co_u32_e32 v38, vcc, s19, v36
	v_ashrrev_i32_e32 v63, 7, v62
	s_nop 0
	v_addc_co_u32_e32 v39, vcc, 0, v37, vcc
	v_add_co_u32_e32 v36, vcc, s20, v36
	v_and_b32_e32 v64, 15, v62
	s_nop 0
	v_addc_co_u32_e32 v37, vcc, 0, v37, vcc
	global_load_dwordx4 v[40:43], v[38:39], off
	s_nop 0
	global_load_dwordx4 v[36:39], v[36:37], off
	v_add_u32_e32 v62, s23, v71
	v_add_u32_e32 v84, v62, v188
	v_add_u32_e32 v86, v62, v192
	v_add_u32_e32 v82, v62, v193
	v_add_u32_e32 v236, v62, v196
	v_mul_lo_u32 v62, v63, s21
	v_add_u32_e32 v189, 0, v71
	v_or_b32_e32 v62, v62, v64
	v_add_u32_e32 v72, 0x16c00, v189
	v_lshlrev_b32_e32 v63, 1, v67
	v_mul_lo_u32 v62, v62, s22
	v_add_u32_e32 v85, v72, v188
	v_add_u32_e32 v87, v72, v192
	v_add_u32_e32 v83, v72, v193
	v_add_u32_e32 v237, v72, v196
	v_add3_u32 v62, 0, v63, v62
	ds_read_b64_tr_b16 v[100:101], v84
	ds_read_b64_tr_b16 v[102:103], v85
	ds_read_b64_tr_b16 v[104:105], v86
	ds_read_b64_tr_b16 v[106:107], v87
	ds_read_b128 v[64:67], v62
	ds_read_b64_tr_b16 v[108:109], v82
	ds_read_b64_tr_b16 v[110:111], v83
	ds_read_b128 v[112:115], v62 offset:2304
	ds_read_b64_tr_b16 v[120:121], v236
	ds_read_b64_tr_b16 v[122:123], v237
	v_add3_u32 v63, 0, v172, v70
	v_or_b32_e32 v197, 0x2000, v71
	v_add_u32_e32 v72, 0x18c00, v189
	s_waitcnt lgkmcnt(5)
	v_mfma_f32_16x16x32_bf16 v[116:119], v[100:103], v[64:67], 0
	v_add3_u32 v79, 0, v69, v68
	v_add_u32_e32 v68, s24, v71
	ds_read_b128 v[176:179], v62 offset:4608
	ds_read_b128 v[180:183], v62 offset:6912
	v_mfma_f32_16x16x32_bf16 v[124:127], v[104:107], v[64:67], 0
	v_add3_u32 v99, s24, v172, v70
	v_add_u32_e32 v98, 0x1b800, v63
	v_add_u32_e32 v95, 0x1c800, v63
	s_waitcnt lgkmcnt(5)
	v_mfma_f32_16x16x32_bf16 v[128:131], v[108:111], v[64:67], 0
	v_add_u32_e32 v92, 0x1d800, v63
	v_add3_u32 v91, s23, v188, v197
	v_add_u32_e32 v93, v72, v188
	s_waitcnt lgkmcnt(2)
	v_mfma_f32_16x16x32_bf16 v[152:155], v[120:123], v[64:67], 0
	v_add_u32_e32 v64, 0x1ac00, v189
	v_add_u32_e32 v66, 0x1cc00, v189
	v_add3_u32 v89, s23, v192, v197
	v_add_u32_e32 v90, v72, v192
	v_add3_u32 v88, s23, v193, v197
	v_add_u32_e32 v94, v72, v193
	v_add3_u32 v96, s23, v196, v197
	v_add_u32_e32 v97, v72, v196
	v_add_u32_e32 v77, v68, v188
	v_add_u32_e32 v78, v64, v188
	v_add_u32_e32 v74, v68, v192
	v_mfma_f32_16x16x32_bf16 v[164:167], v[100:103], v[112:115], 0
	v_add_u32_e32 v75, v64, v192
	v_add_u32_e32 v76, v68, v193
	v_add_u32_e32 v71, v64, v193
	v_mfma_f32_16x16x32_bf16 v[168:171], v[104:107], v[112:115], 0
	v_add_u32_e32 v72, v68, v196
	v_add_u32_e32 v73, v64, v196
	v_add3_u32 v238, s23, v172, v70
	v_mfma_f32_16x16x32_bf16 v[172:175], v[108:111], v[112:115], 0
	v_add_u32_e32 v239, 0x17800, v63
	v_add_u32_e32 v240, 0x18800, v63
	v_add_u32_e32 v241, 0x19800, v63
	v_mfma_f32_16x16x32_bf16 v[112:115], v[120:123], v[112:115], 0
	v_add3_u32 v68, s24, v188, v197
	v_add_u32_e32 v70, v66, v188
	v_add3_u32 v67, s24, v192, v197
	v_add_u32_e32 v69, v66, v192
	v_add3_u32 v63, s24, v193, v197
	v_add_u32_e32 v64, v66, v193
	v_add3_u32 v65, s24, v196, v197
	v_add_u32_e32 v66, v66, v196
	ds_read_b128 v[196:199], v62 offset:9216
	v_add_u32_e32 v80, 0x12000, v79
	v_add_u32_e32 v81, 0x14400, v79
	s_waitcnt vmcnt(12)
	v_cvt_pk_bf16_f32 v12, v12, v13
	v_cvt_pk_bf16_f32 v13, v14, v15
	s_waitcnt vmcnt(11)
	v_cvt_pk_bf16_f32 v8, v8, v9
	v_cvt_pk_bf16_f32 v9, v10, v11
	v_readlane_b32 s37, v253, 5
	v_readlane_b32 s38, v253, 6
	v_readlane_b32 s39, v253, 7
	v_readlane_b32 s40, v253, 8
	v_readlane_b32 s41, v253, 9
	v_readlane_b32 s42, v253, 10
	v_readlane_b32 s43, v253, 11
	v_readlane_b32 s44, v253, 12
	v_readlane_b32 s45, v253, 13
	v_readlane_b32 s46, v253, 14
	v_readlane_b32 s47, v253, 15
	v_readlane_b32 s50, v253, 18
	v_readlane_b32 s51, v253, 19
	s_waitcnt lgkmcnt(2)
	v_mfma_f32_16x16x32_bf16 v[184:187], v[100:103], v[176:179], 0
	ds_write_b64 v99, v[12:13]
	ds_write_b64 v98, v[8:9]
	v_mfma_f32_16x16x32_bf16 v[188:191], v[104:107], v[176:179], 0
	v_mfma_f32_16x16x32_bf16 v[192:195], v[108:111], v[176:179], 0
	v_mfma_f32_16x16x32_bf16 v[176:179], v[120:123], v[176:179], 0
	ds_read_b128 v[204:207], v62 offset:64
	ds_read_b128 v[208:211], v62 offset:2368
	s_waitcnt vmcnt(9)
	v_cvt_pk_bf16_f32 v0, v0, v1
	v_cvt_pk_bf16_f32 v1, v2, v3
	s_waitcnt lgkmcnt(5)
	v_mfma_f32_16x16x32_bf16 v[8:11], v[100:103], v[180:183], 0
	ds_read_b128 v[212:215], v62 offset:4672
	v_cvt_pk_bf16_f32 v216, v4, v5
	v_cvt_pk_bf16_f32 v217, v6, v7
	v_mfma_f32_16x16x32_bf16 v[12:15], v[104:107], v[180:183], 0
	ds_write_b64 v92, v[0:1]
	ds_write_b64 v95, v[216:217]
	s_waitcnt lgkmcnt(7)
	v_mfma_f32_16x16x32_bf16 v[100:103], v[100:103], v[196:199], 0
	v_mfma_f32_16x16x32_bf16 v[104:107], v[104:107], v[196:199], 0
	v_mfma_f32_16x16x32_bf16 v[4:7], v[108:111], v[196:199], 0
	v_mfma_f32_16x16x32_bf16 v[0:3], v[120:123], v[196:199], 0
	v_mfma_f32_16x16x32_bf16 v[200:203], v[108:111], v[180:183], 0
	v_mfma_f32_16x16x32_bf16 v[180:183], v[120:123], v[180:183], 0
	ds_read_b64_tr_b16 v[108:109], v91
	ds_read_b64_tr_b16 v[110:111], v93
	ds_read_b64_tr_b16 v[120:121], v89
	ds_read_b64_tr_b16 v[122:123], v90
	ds_read_b64_tr_b16 v[196:197], v88
	ds_read_b64_tr_b16 v[198:199], v94
	ds_read_b64_tr_b16 v[216:217], v96
	ds_read_b64_tr_b16 v[218:219], v97
	s_waitcnt lgkmcnt(6)
	v_mfma_f32_16x16x32_bf16 v[116:119], v[108:111], v[204:207], v[116:119]
	s_waitcnt lgkmcnt(4)
	v_mfma_f32_16x16x32_bf16 v[124:127], v[120:123], v[204:207], v[124:127]
	s_waitcnt lgkmcnt(2)
	v_mfma_f32_16x16x32_bf16 v[128:131], v[196:199], v[204:207], v[128:131]
	s_waitcnt lgkmcnt(0)
	v_mfma_f32_16x16x32_bf16 v[152:155], v[216:219], v[204:207], v[152:155]
	v_mfma_f32_16x16x32_bf16 v[164:167], v[108:111], v[208:211], v[164:167]
	v_mfma_f32_16x16x32_bf16 v[168:171], v[120:123], v[208:211], v[168:171]
	v_mfma_f32_16x16x32_bf16 v[172:175], v[196:199], v[208:211], v[172:175]
	v_mfma_f32_16x16x32_bf16 v[112:115], v[216:219], v[208:211], v[112:115]
	ds_read_b128 v[204:207], v62 offset:6976
	ds_read_b128 v[208:211], v62 offset:9280
	s_waitcnt vmcnt(8)
	ds_write_b128 v79, v[24:27] offset:46080
	s_waitcnt vmcnt(7)
	ds_write_b128 v79, v[28:31] offset:55296
	v_mfma_f32_16x16x32_bf16 v[24:27], v[216:219], v[212:215], v[176:179]
	v_mfma_f32_16x16x32_bf16 v[184:187], v[108:111], v[212:215], v[184:187]
	v_mfma_f32_16x16x32_bf16 v[188:191], v[120:123], v[212:215], v[188:191]
	v_mfma_f32_16x16x32_bf16 v[192:195], v[196:199], v[212:215], v[192:195]
	s_waitcnt lgkmcnt(3)
	v_mfma_f32_16x16x32_bf16 v[8:11], v[108:111], v[204:207], v[8:11]
	v_mfma_f32_16x16x32_bf16 v[28:31], v[120:123], v[204:207], v[12:15]
	v_mfma_f32_16x16x32_bf16 v[176:179], v[196:199], v[204:207], v[200:203]
	v_mfma_f32_16x16x32_bf16 v[180:183], v[216:219], v[204:207], v[180:183]
	s_waitcnt lgkmcnt(2)
	v_mfma_f32_16x16x32_bf16 v[100:103], v[108:111], v[208:211], v[100:103]
	v_mfma_f32_16x16x32_bf16 v[104:107], v[120:123], v[208:211], v[104:107]
	global_load_dwordx4 v[108:111], v[52:53], off offset:256
	global_load_dwordx4 v[120:123], v[54:55], off offset:256
	global_load_dwordx4 v[200:203], v[56:57], off offset:256
	global_load_dwordx4 v[204:207], v[58:59], off offset:256
	global_load_dwordx4 v[212:215], v[60:61], off offset:256
	s_waitcnt vmcnt(11)
	ds_write_b128 v79, v[16:19] offset:64512
	s_waitcnt vmcnt(10)
	ds_write_b128 v80, v[20:23]
	s_waitcnt vmcnt(9)
	ds_write_b128 v81, v[32:35]
	v_mfma_f32_16x16x32_bf16 v[4:7], v[196:199], v[208:211], v[4:7]
	v_mfma_f32_16x16x32_bf16 v[0:3], v[216:219], v[208:211], v[0:3]
	s_waitcnt lgkmcnt(0)
	s_barrier
	ds_read_b64_tr_b16 v[16:17], v77
	ds_read_b64_tr_b16 v[18:19], v78
	ds_read_b128 v[12:15], v62 offset:46080
	ds_read_b64_tr_b16 v[20:21], v74
	ds_read_b64_tr_b16 v[22:23], v75
	ds_read_b64_tr_b16 v[196:197], v76
	ds_read_b128 v[32:35], v62 offset:48384
	ds_read_b128 v[208:211], v62 offset:55296
	ds_read_b64_tr_b16 v[198:199], v71
	ds_read_b64_tr_b16 v[216:217], v72
	ds_read_b64_tr_b16 v[218:219], v73
	s_waitcnt lgkmcnt(8)
	v_mfma_f32_16x16x32_bf16 v[116:119], v[16:19], v[12:15], v[116:119]
	ds_read_b128 v[220:223], v62 offset:50688
	s_waitcnt vmcnt(8)
	v_cvt_pk_bf16_f32 v48, v48, v49
	v_cvt_pk_bf16_f32 v49, v50, v51
	s_waitcnt lgkmcnt(7)
	v_mfma_f32_16x16x32_bf16 v[124:127], v[20:23], v[12:15], v[124:127]
	s_waitcnt vmcnt(7)
	v_cvt_pk_bf16_f32 v44, v44, v45
	v_cvt_pk_bf16_f32 v45, v46, v47
	s_waitcnt lgkmcnt(3)
	v_mfma_f32_16x16x32_bf16 v[128:131], v[196:199], v[12:15], v[128:131]
	s_waitcnt lgkmcnt(1)
	v_mfma_f32_16x16x32_bf16 v[152:155], v[216:219], v[12:15], v[152:155]
	v_lshl_add_u64 v[12:13], s[8:9], 0, v[146:147]
	v_lshl_add_u64 v[12:13], v[12:13], 0, s[10:11]
	v_lshl_add_u64 v[12:13], v[12:13], 0, v[132:133]
	v_lshl_add_u64 v[12:13], v[12:13], 0, v[148:149]
	v_lshl_add_u64 v[12:13], v[12:13], 0, v[150:151]
	v_add_co_u32_e32 v14, vcc, s18, v12
	v_mfma_f32_16x16x32_bf16 v[164:167], v[16:19], v[32:35], v[164:167]
	s_nop 0
	v_addc_co_u32_e32 v15, vcc, 0, v13, vcc
	global_load_dwordx4 v[224:227], v[12:13], off
	global_load_dwordx4 v[228:231], v[14:15], off
	v_add_co_u32_e32 v14, vcc, s19, v12
	v_mfma_f32_16x16x32_bf16 v[168:171], v[20:23], v[32:35], v[168:171]
	s_nop 0
	v_addc_co_u32_e32 v15, vcc, 0, v13, vcc
	v_add_co_u32_e32 v12, vcc, s20, v12
	v_mfma_f32_16x16x32_bf16 v[172:175], v[196:199], v[32:35], v[172:175]
	s_nop 0
	v_addc_co_u32_e32 v13, vcc, 0, v13, vcc
	ds_read_b128 v[232:235], v62 offset:52992
	v_mfma_f32_16x16x32_bf16 v[112:115], v[216:219], v[32:35], v[112:115]
	global_load_dwordx4 v[32:35], v[14:15], off
	s_nop 0
	global_load_dwordx4 v[12:15], v[12:13], off
	ds_write_b64 v238, v[48:49]
	ds_write_b64 v239, v[44:45]
	s_waitcnt lgkmcnt(3)
	v_mfma_f32_16x16x32_bf16 v[24:27], v[216:219], v[220:223], v[24:27]
	v_mfma_f32_16x16x32_bf16 v[184:187], v[16:19], v[220:223], v[184:187]
	v_mfma_f32_16x16x32_bf16 v[188:191], v[20:23], v[220:223], v[188:191]
	v_mfma_f32_16x16x32_bf16 v[192:195], v[196:199], v[220:223], v[192:195]
	s_waitcnt lgkmcnt(2)
	v_mfma_f32_16x16x32_bf16 v[8:11], v[16:19], v[232:235], v[8:11]
	v_mfma_f32_16x16x32_bf16 v[28:31], v[20:23], v[232:235], v[28:31]
	v_mfma_f32_16x16x32_bf16 v[44:47], v[196:199], v[232:235], v[176:179]
	v_mfma_f32_16x16x32_bf16 v[16:19], v[16:19], v[208:211], v[100:103]
	s_nop 2
	ds_read_b128 v[100:103], v62 offset:46144
	ds_read_b128 v[176:179], v62 offset:48448
	v_mfma_f32_16x16x32_bf16 v[20:23], v[20:23], v[208:211], v[104:107]
	s_nop 2
	ds_read_b128 v[104:107], v62 offset:50752
	v_mfma_f32_16x16x32_bf16 v[48:51], v[216:219], v[232:235], v[180:183]
	s_waitcnt vmcnt(10)
	s_nop 1
	v_cvt_pk_bf16_f32 v180, v40, v41
	v_cvt_pk_bf16_f32 v181, v42, v43
	v_mfma_f32_16x16x32_bf16 v[40:43], v[196:199], v[208:211], v[4:7]
	ds_write_b64 v240, v[180:181]
	s_waitcnt vmcnt(9)
	s_nop 0
	v_cvt_pk_bf16_f32 v4, v36, v37
	v_cvt_pk_bf16_f32 v5, v38, v39
	v_mfma_f32_16x16x32_bf16 v[36:39], v[216:219], v[208:211], v[0:3]
	ds_write_b64 v241, v[4:5]
	s_nop 1
	ds_read_b64_tr_b16 v[0:1], v68
	ds_read_b64_tr_b16 v[2:3], v70
	ds_read_b64_tr_b16 v[4:5], v67
	ds_read_b64_tr_b16 v[6:7], v69
	ds_read_b64_tr_b16 v[180:181], v63
	ds_read_b64_tr_b16 v[182:183], v64
	ds_read_b64_tr_b16 v[196:197], v65
	ds_read_b64_tr_b16 v[198:199], v66
	s_waitcnt lgkmcnt(6)
	v_mfma_f32_16x16x32_bf16 v[116:119], v[0:3], v[100:103], v[116:119]
	s_waitcnt lgkmcnt(4)
	v_mfma_f32_16x16x32_bf16 v[124:127], v[4:7], v[100:103], v[124:127]
	s_waitcnt lgkmcnt(2)
	v_mfma_f32_16x16x32_bf16 v[128:131], v[180:183], v[100:103], v[128:131]
	s_waitcnt lgkmcnt(0)
	v_mfma_f32_16x16x32_bf16 v[100:103], v[196:199], v[100:103], v[152:155]
	v_mfma_f32_16x16x32_bf16 v[152:155], v[0:3], v[176:179], v[164:167]
	v_mfma_f32_16x16x32_bf16 v[164:167], v[4:7], v[176:179], v[168:171]
	v_mfma_f32_16x16x32_bf16 v[168:171], v[180:183], v[176:179], v[172:175]
	v_mfma_f32_16x16x32_bf16 v[112:115], v[196:199], v[176:179], v[112:115]
	v_mfma_f32_16x16x32_bf16 v[172:175], v[0:3], v[104:107], v[184:187]
	v_mfma_f32_16x16x32_bf16 v[176:179], v[4:7], v[104:107], v[188:191]
	v_mfma_f32_16x16x32_bf16 v[184:187], v[180:183], v[104:107], v[192:195]
	s_nop 1
	ds_read_b128 v[188:191], v62 offset:53056
	ds_read_b128 v[192:195], v62 offset:55360
	s_waitcnt vmcnt(8)
	ds_write_b128 v79, v[108:111]
	s_waitcnt vmcnt(7)
	ds_write_b128 v79, v[120:123] offset:9216
	v_mfma_f32_16x16x32_bf16 v[104:107], v[196:199], v[104:107], v[24:27]
	s_waitcnt lgkmcnt(3)
	v_mfma_f32_16x16x32_bf16 v[108:111], v[0:3], v[188:191], v[8:11]
	v_mfma_f32_16x16x32_bf16 v[120:123], v[4:7], v[188:191], v[28:31]
	v_mfma_f32_16x16x32_bf16 v[44:47], v[180:183], v[188:191], v[44:47]
	v_mfma_f32_16x16x32_bf16 v[48:51], v[196:199], v[188:191], v[48:51]
	s_waitcnt lgkmcnt(2)
	v_mfma_f32_16x16x32_bf16 v[188:191], v[0:3], v[192:195], v[16:19]
	v_mfma_f32_16x16x32_bf16 v[208:211], v[4:7], v[192:195], v[20:23]
	global_load_dwordx4 v[216:219], v[52:53], off offset:384
	s_nop 0
	global_load_dwordx4 v[52:55], v[54:55], off offset:384
	s_nop 0
	global_load_dwordx4 v[0:3], v[56:57], off offset:384
	global_load_dwordx4 v[4:7], v[58:59], off offset:384
	global_load_dwordx4 v[8:11], v[60:61], off offset:384
	s_waitcnt vmcnt(11)
	ds_write_b128 v79, v[200:203] offset:18432
	s_waitcnt vmcnt(10)
	ds_write_b128 v79, v[204:207] offset:27648
	s_waitcnt vmcnt(9)
	ds_write_b128 v79, v[212:215] offset:36864
	v_mfma_f32_16x16x32_bf16 v[40:43], v[180:183], v[192:195], v[40:43]
	v_mfma_f32_16x16x32_bf16 v[36:39], v[196:199], v[192:195], v[36:39]
	s_cmpk_lt_i32 s26, 0x100
	s_cselect_b32 s8, s26, 1
	s_waitcnt lgkmcnt(0)
	s_barrier
	ds_read_b64_tr_b16 v[56:57], v84
	ds_read_b64_tr_b16 v[58:59], v85
	ds_read_b64_tr_b16 v[84:85], v86
	ds_read_b64_tr_b16 v[86:87], v87
	ds_read_b128 v[16:19], v62
	ds_read_b64_tr_b16 v[180:181], v82
	ds_read_b64_tr_b16 v[182:183], v83
	ds_read_b128 v[20:23], v62 offset:2304
	ds_read_b64_tr_b16 v[192:193], v236
	ds_read_b64_tr_b16 v[194:195], v237
	s_cselect_b32 s10, s17, s49
	s_cselect_b32 s11, s16, s48
	s_ashr_i32 s9, s8, 31
	s_lshl_b64 s[8:9], s[8:9], 20
	s_add_u32 s8, s11, s8
	s_addc_u32 s9, s10, s9
	s_lshl_b32 s10, s27, 7
	s_ashr_i32 s11, s10, 31
	s_waitcnt lgkmcnt(5)
	v_mfma_f32_16x16x32_bf16 v[116:119], v[56:59], v[16:19], v[116:119]
	s_lshl_b64 s[10:11], s[10:11], 2
	ds_read_b128 v[196:199], v62 offset:4608
	s_waitcnt vmcnt(8)
	v_cvt_pk_bf16_f32 v60, v224, v225
	v_mfma_f32_16x16x32_bf16 v[124:127], v[84:87], v[16:19], v[124:127]
	v_cvt_pk_bf16_f32 v61, v226, v227
	s_waitcnt lgkmcnt(4)
	v_mfma_f32_16x16x32_bf16 v[128:131], v[180:183], v[16:19], v[128:131]
	s_waitcnt lgkmcnt(1)
	v_mfma_f32_16x16x32_bf16 v[100:103], v[192:195], v[16:19], v[100:103]
	v_lshl_add_u64 v[16:17], s[8:9], 0, v[136:137]
	v_lshl_add_u64 v[16:17], v[16:17], 0, s[10:11]
	v_lshl_add_u64 v[16:17], v[16:17], 0, v[132:133]
	v_lshl_add_u64 v[16:17], v[16:17], 0, v[148:149]
	v_lshl_add_u64 v[24:25], v[16:17], 0, v[150:151]
	v_add_co_u32_e32 v16, vcc, s18, v24
	v_mfma_f32_16x16x32_bf16 v[152:155], v[56:59], v[20:23], v[152:155]
	s_nop 0
	v_addc_co_u32_e32 v17, vcc, 0, v25, vcc
	v_add_co_u32_e32 v26, vcc, s19, v24
	v_mfma_f32_16x16x32_bf16 v[164:167], v[84:87], v[20:23], v[164:167]
	s_nop 0
	v_addc_co_u32_e32 v27, vcc, 0, v25, vcc
	v_mfma_f32_16x16x32_bf16 v[168:171], v[180:183], v[20:23], v[168:171]
	v_mfma_f32_16x16x32_bf16 v[112:115], v[192:195], v[20:23], v[112:115]
	global_load_dwordx4 v[20:23], v[24:25], off
	s_nop 0
	global_load_dwordx4 v[16:19], v[16:17], off
	v_add_co_u32_e32 v24, vcc, s20, v24
	ds_read_b128 v[200:203], v62 offset:6912
	s_nop 0
	v_addc_co_u32_e32 v25, vcc, 0, v25, vcc
	global_load_dwordx4 v[28:31], v[26:27], off
	s_nop 0
	global_load_dwordx4 v[24:27], v[24:25], off
	ds_read_b128 v[204:207], v62 offset:9216
	s_waitcnt lgkmcnt(2)
	v_mfma_f32_16x16x32_bf16 v[104:107], v[192:195], v[196:199], v[104:107]
	ds_write_b64 v99, v[60:61]
	s_waitcnt vmcnt(11)
	v_cvt_pk_bf16_f32 v60, v228, v229
	v_cvt_pk_bf16_f32 v61, v230, v231
	v_mfma_f32_16x16x32_bf16 v[172:175], v[56:59], v[196:199], v[172:175]
	ds_write_b64 v98, v[60:61]
	v_mfma_f32_16x16x32_bf16 v[176:179], v[84:87], v[196:199], v[176:179]
	v_mfma_f32_16x16x32_bf16 v[184:187], v[180:183], v[196:199], v[184:187]
	s_waitcnt lgkmcnt(3)
	v_mfma_f32_16x16x32_bf16 v[108:111], v[56:59], v[200:203], v[108:111]
	s_waitcnt vmcnt(9)
	v_cvt_pk_bf16_f32 v12, v12, v13
	v_cvt_pk_bf16_f32 v13, v14, v15
	v_cvt_pk_bf16_f32 v32, v32, v33
	s_waitcnt lgkmcnt(2)
	v_mfma_f32_16x16x32_bf16 v[56:59], v[56:59], v[204:207], v[188:191]
	s_nop 2
	ds_read_b128 v[188:191], v62 offset:64
	ds_read_b128 v[196:199], v62 offset:2368
	v_cvt_pk_bf16_f32 v33, v34, v35
	v_mfma_f32_16x16x32_bf16 v[120:123], v[84:87], v[200:203], v[120:123]
	v_mfma_f32_16x16x32_bf16 v[44:47], v[180:183], v[200:203], v[44:47]
	v_mfma_f32_16x16x32_bf16 v[48:51], v[192:195], v[200:203], v[48:51]
	ds_read_b128 v[200:203], v62 offset:4672
	ds_write_b64 v92, v[12:13]
	ds_write_b64 v95, v[32:33]
	v_mfma_f32_16x16x32_bf16 v[82:85], v[84:87], v[204:207], v[208:211]
	v_mfma_f32_16x16x32_bf16 v[40:43], v[180:183], v[204:207], v[40:43]
	v_mfma_f32_16x16x32_bf16 v[12:15], v[192:195], v[204:207], v[36:39]
	ds_read_b64_tr_b16 v[32:33], v91
	ds_read_b64_tr_b16 v[34:35], v93
	ds_read_b64_tr_b16 v[180:181], v89
	ds_read_b64_tr_b16 v[182:183], v90
	ds_read_b64_tr_b16 v[86:87], v88
	ds_read_b64_tr_b16 v[88:89], v94
	ds_read_b64_tr_b16 v[94:95], v96
	ds_read_b64_tr_b16 v[96:97], v97
	s_waitcnt lgkmcnt(6)
	v_mfma_f32_16x16x32_bf16 v[90:93], v[32:35], v[188:191], v[116:119]
	s_waitcnt lgkmcnt(4)
	v_mfma_f32_16x16x32_bf16 v[116:119], v[180:183], v[188:191], v[124:127]
	s_waitcnt lgkmcnt(2)
	v_mfma_f32_16x16x32_bf16 v[124:127], v[86:89], v[188:191], v[128:131]
	v_mfma_f32_16x16x32_bf16 v[128:131], v[32:35], v[196:199], v[152:155]
	v_mfma_f32_16x16x32_bf16 v[152:155], v[180:183], v[196:199], v[164:167]
	v_mfma_f32_16x16x32_bf16 v[164:167], v[86:89], v[196:199], v[168:171]
	v_mfma_f32_16x16x32_bf16 v[168:171], v[32:35], v[200:203], v[172:175]
	v_mfma_f32_16x16x32_bf16 v[172:175], v[180:183], v[200:203], v[176:179]
	v_mfma_f32_16x16x32_bf16 v[176:179], v[86:89], v[200:203], v[184:187]
	ds_read_b128 v[36:39], v62 offset:6976
	s_nop 1
	ds_read_b128 v[184:187], v62 offset:9280
	s_waitcnt vmcnt(8)
	ds_write_b128 v79, v[216:219] offset:46080
	s_waitcnt vmcnt(7)
	ds_write_b128 v79, v[52:55] offset:55296
	s_waitcnt lgkmcnt(4)
	v_mfma_f32_16x16x32_bf16 v[98:101], v[94:97], v[188:191], v[100:103]
	v_mfma_f32_16x16x32_bf16 v[112:115], v[94:97], v[196:199], v[112:115]
	v_mfma_f32_16x16x32_bf16 v[52:55], v[94:97], v[200:203], v[104:107]
	v_sub_u32_e32 v60, v163, v143
	v_xad_u32 v192, s28, -1, v60
	v_add_u32_e32 v61, s28, v162
	s_waitcnt lgkmcnt(3)
	v_mfma_f32_16x16x32_bf16 v[102:105], v[32:35], v[36:39], v[108:111]
	v_min_i32_e32 v60, 0, v192
	s_nop 1
	v_add_u32_e32 v110, v61, v143
	v_mfma_f32_16x16x32_bf16 v[106:109], v[180:183], v[36:39], v[120:123]
	v_add_u32_e32 v60, v60, v110
	v_ashrrev_i32_e32 v61, 31, v60
	v_lshlrev_b64 v[60:61], 9, v[60:61]
	v_mfma_f32_16x16x32_bf16 v[120:123], v[86:89], v[36:39], v[44:47]
	s_nop 2
	v_min_i32_e32 v46, 64, v192
	v_add_u32_e32 v46, v46, v110
	v_ashrrev_i32_e32 v47, 31, v46
	v_lshl_add_u64 v[44:45], v[134:135], 0, v[60:61]
	v_mfma_f32_16x16x32_bf16 v[188:191], v[94:97], v[36:39], v[48:51]
	v_lshlrev_b64 v[36:37], 9, v[46:47]
	v_lshl_add_u64 v[46:47], v[134:135], 0, v[36:37]
	s_waitcnt lgkmcnt(2)
	v_mfma_f32_16x16x32_bf16 v[56:59], v[32:35], v[184:187], v[56:59]
	global_load_dwordx4 v[36:39], v[44:45], off
	global_load_dwordx4 v[32:35], v[46:47], off
	v_min_i32_e32 v44, 0x80, v192
	v_min_i32_e32 v48, 0x100, v192
	v_mfma_f32_16x16x32_bf16 v[86:89], v[86:89], v[184:187], v[40:43]
	v_add_u32_e32 v44, v44, v110
	v_add_u32_e32 v48, v48, v110
	v_ashrrev_i32_e32 v45, 31, v44
	v_min_i32_e32 v42, 0xc0, v192
	v_add_u32_e32 v42, v42, v110
	v_ashrrev_i32_e32 v43, 31, v42
	v_ashrrev_i32_e32 v49, 31, v48
	v_lshlrev_b64 v[44:45], 9, v[44:45]
	v_lshlrev_b64 v[42:43], 9, v[42:43]
	v_lshlrev_b64 v[48:49], 9, v[48:49]
	v_lshl_add_u64 v[40:41], v[134:135], 0, v[44:45]
	v_lshl_add_u64 v[42:43], v[134:135], 0, v[42:43]
	v_lshl_add_u64 v[48:49], v[134:135], 0, v[48:49]
	global_load_dwordx4 v[44:47], v[40:41], off
	s_nop 0
	global_load_dwordx4 v[40:43], v[42:43], off
	v_mfma_f32_16x16x32_bf16 v[82:85], v[180:183], v[184:187], v[82:85]
	global_load_dwordx4 v[48:51], v[48:49], off
	s_waitcnt vmcnt(11)
	ds_write_b128 v79, v[0:3] offset:64512
	s_waitcnt vmcnt(10)
	ds_write_b128 v80, v[4:7]
	s_waitcnt vmcnt(9)
	ds_write_b128 v81, v[8:11]
	v_mfma_f32_16x16x32_bf16 v[94:97], v[94:97], v[184:187], v[12:15]
	s_waitcnt lgkmcnt(0)
	s_barrier
	ds_read_b64_tr_b16 v[180:181], v77
	ds_read_b64_tr_b16 v[182:183], v78
	ds_read_b128 v[0:3], v62 offset:46080
	ds_read_b64_tr_b16 v[78:79], v74
	ds_read_b64_tr_b16 v[80:81], v75
	ds_read_b64_tr_b16 v[74:75], v76
	ds_read_b128 v[4:7], v62 offset:48384
	ds_read_b128 v[184:187], v62 offset:55296
	ds_read_b64_tr_b16 v[76:77], v71
	ds_read_b64_tr_b16 v[192:193], v72
	ds_read_b64_tr_b16 v[194:195], v73
	s_waitcnt lgkmcnt(8)
	v_mfma_f32_16x16x32_bf16 v[90:93], v[180:183], v[0:3], v[90:93]
	s_waitcnt lgkmcnt(6)
	v_mfma_f32_16x16x32_bf16 v[116:119], v[78:81], v[0:3], v[116:119]
	s_waitcnt lgkmcnt(2)
	v_mfma_f32_16x16x32_bf16 v[196:199], v[74:77], v[0:3], v[124:127]
	s_waitcnt lgkmcnt(0)
	v_mfma_f32_16x16x32_bf16 v[98:101], v[192:195], v[0:3], v[98:101]
	v_lshl_add_u64 v[0:1], s[8:9], 0, v[138:139]
	v_lshl_add_u64 v[0:1], v[0:1], 0, s[10:11]
	v_lshl_add_u64 v[0:1], v[0:1], 0, v[132:133]
	v_lshl_add_u64 v[0:1], v[0:1], 0, v[148:149]
	v_lshl_add_u64 v[0:1], v[0:1], 0, v[150:151]
	v_add_co_u32_e32 v2, vcc, s18, v0
	ds_read_b128 v[124:127], v62 offset:50688
	s_nop 0
	v_addc_co_u32_e32 v3, vcc, 0, v1, vcc
	global_load_dwordx4 v[12:15], v[0:1], off
	global_load_dwordx4 v[8:11], v[2:3], off
	v_add_co_u32_e32 v2, vcc, s19, v0
	v_mfma_f32_16x16x32_bf16 v[200:203], v[180:183], v[4:7], v[128:131]
	s_nop 0
	v_addc_co_u32_e32 v3, vcc, 0, v1, vcc
	v_add_co_u32_e32 v0, vcc, s20, v0
	v_mfma_f32_16x16x32_bf16 v[152:155], v[78:81], v[4:7], v[152:155]
	s_nop 0
	v_addc_co_u32_e32 v1, vcc, 0, v1, vcc
	v_mfma_f32_16x16x32_bf16 v[164:167], v[74:77], v[4:7], v[164:167]
	v_mfma_f32_16x16x32_bf16 v[204:207], v[192:195], v[4:7], v[112:115]
	s_nop 2
	ds_read_b128 v[110:113], v62 offset:52992
	global_load_dwordx4 v[4:7], v[2:3], off
	s_nop 0
	global_load_dwordx4 v[0:3], v[0:1], off
	s_waitcnt lgkmcnt(1)
	v_mfma_f32_16x16x32_bf16 v[52:55], v[192:195], v[124:127], v[52:55]
	v_mfma_f32_16x16x32_bf16 v[168:171], v[180:183], v[124:127], v[168:171]
	v_mfma_f32_16x16x32_bf16 v[172:175], v[78:81], v[124:127], v[172:175]
	v_mfma_f32_16x16x32_bf16 v[176:179], v[74:77], v[124:127], v[176:179]
	s_waitcnt lgkmcnt(0)
	v_mfma_f32_16x16x32_bf16 v[208:211], v[180:183], v[110:113], v[102:105]
	v_mfma_f32_16x16x32_bf16 v[212:215], v[78:81], v[110:113], v[106:109]
	v_mfma_f32_16x16x32_bf16 v[216:219], v[74:77], v[110:113], v[120:123]
	v_mfma_f32_16x16x32_bf16 v[56:59], v[180:183], v[184:187], v[56:59]
	v_mfma_f32_16x16x32_bf16 v[180:183], v[78:81], v[184:187], v[82:85]
	v_mfma_f32_16x16x32_bf16 v[220:223], v[74:77], v[184:187], v[86:89]
	ds_read_b128 v[72:75], v62 offset:46144
	ds_read_b128 v[76:79], v62 offset:48448
	ds_read_b128 v[80:83], v62 offset:50752
	v_mfma_f32_16x16x32_bf16 v[188:191], v[192:195], v[110:113], v[188:191]
	v_mfma_f32_16x16x32_bf16 v[184:187], v[192:195], v[184:187], v[94:97]
	ds_read_b64_tr_b16 v[192:193], v68
	ds_read_b64_tr_b16 v[194:195], v70
	ds_read_b64_tr_b16 v[224:225], v67
	ds_read_b64_tr_b16 v[226:227], v69
	ds_read_b64_tr_b16 v[228:229], v63
	ds_read_b64_tr_b16 v[230:231], v64
	ds_read_b64_tr_b16 v[232:233], v65
	ds_read_b64_tr_b16 v[234:235], v66
	s_waitcnt lgkmcnt(6)
	v_mfma_f32_16x16x32_bf16 v[124:127], v[192:195], v[72:75], v[90:93]
	s_waitcnt lgkmcnt(4)
	v_mfma_f32_16x16x32_bf16 v[108:111], v[224:227], v[76:79], v[152:155]
	ds_read_b128 v[64:67], v62 offset:53056
	s_nop 1
	ds_read_b128 v[152:155], v62 offset:55360
	v_mfma_f32_16x16x32_bf16 v[128:131], v[224:227], v[72:75], v[116:119]
	s_waitcnt lgkmcnt(4)
	v_mfma_f32_16x16x32_bf16 v[120:123], v[228:231], v[72:75], v[196:199]
	s_waitcnt lgkmcnt(2)
	v_mfma_f32_16x16x32_bf16 v[116:119], v[232:235], v[72:75], v[98:101]
	v_mfma_f32_16x16x32_bf16 v[112:115], v[192:195], v[76:79], v[200:203]
	v_mfma_f32_16x16x32_bf16 v[104:107], v[228:231], v[76:79], v[164:167]
	v_mfma_f32_16x16x32_bf16 v[100:103], v[232:235], v[76:79], v[204:207]
	v_mfma_f32_16x16x32_bf16 v[96:99], v[192:195], v[80:83], v[168:171]
	v_mfma_f32_16x16x32_bf16 v[92:95], v[224:227], v[80:83], v[172:175]
	v_mfma_f32_16x16x32_bf16 v[84:87], v[228:231], v[80:83], v[176:179]
	v_mfma_f32_16x16x32_bf16 v[88:91], v[232:235], v[80:83], v[52:55]
	s_waitcnt lgkmcnt(1)
	v_mfma_f32_16x16x32_bf16 v[80:83], v[192:195], v[64:67], v[208:211]
	v_mfma_f32_16x16x32_bf16 v[76:79], v[224:227], v[64:67], v[212:215]
	v_mfma_f32_16x16x32_bf16 v[72:75], v[228:231], v[64:67], v[216:219]
	v_mfma_f32_16x16x32_bf16 v[68:71], v[232:235], v[64:67], v[188:191]
	s_waitcnt lgkmcnt(0)
	v_mfma_f32_16x16x32_bf16 v[64:67], v[192:195], v[152:155], v[56:59]
	v_mfma_f32_16x16x32_bf16 v[60:63], v[224:227], v[152:155], v[180:183]
	v_mfma_f32_16x16x32_bf16 v[56:59], v[228:231], v[152:155], v[220:223]
	v_mfma_f32_16x16x32_bf16 v[52:55], v[232:235], v[152:155], v[184:187]
	v_add_u32_e32 v149, s14, v157
	v_cmp_lt_i32_e32 vcc, v149, v156
	v_lshlrev_b32_e32 v154, 1, v140
	v_lshlrev_b32_e32 v152, 1, v142
	v_and_b32_e32 v248, 16, v142
	v_sub_u32_e32 v152, v152, v248
	s_and_saveexec_b64 s[8:9], vcc
	s_cbranch_execz .LBB0_2487
	v_add_u32_e32 v164, v141, v149
	v_ashrrev_i32_e32 v165, 31, v164
	v_readlane_b32 s10, v254, 3
	v_lshlrev_b64 v[164:165], 11, v[164:165]
	v_readlane_b32 s11, v254, 4
	v_mov_b32_e32 v155, v133
	v_mov_b32_e32 v153, v133
	v_lshl_add_u64 v[164:165], s[10:11], 0, v[164:165]
	v_lshl_add_u64 v[164:165], s[6:7], 1, v[164:165]
	v_lshl_add_u64 v[164:165], v[164:165], 0, v[154:155]
	v_lshl_add_u64 v[164:165], v[164:165], 0, v[152:153]
	v_cvt_pk_bf16_f32 v124, v124, v125
	v_cvt_pk_bf16_f32 v125, v126, v127
	v_cvt_pk_bf16_f32 v126, v128, v129
	v_cvt_pk_bf16_f32 v127, v130, v131
	v_cvt_pk_bf16_f32 v120, v120, v121
	v_cvt_pk_bf16_f32 v121, v122, v123
	v_cvt_pk_bf16_f32 v122, v116, v117
	v_cvt_pk_bf16_f32 v123, v118, v119
	s_nop 1
	v_permlane16_swap_b32 v124, v120
	v_permlane16_swap_b32 v125, v121
	v_permlane16_swap_b32 v126, v122
	v_permlane16_swap_b32 v127, v123
	global_store_dwordx4 v[164:165], v[124:127], off
	global_store_dwordx4 v[164:165], v[120:123], off offset:32
.LBB0_2487:
	s_or_b64 exec, exec, s[8:9]
	v_add_u32_e32 v116, s14, v158
	v_cmp_lt_i32_e32 vcc, v116, v156
	s_and_saveexec_b64 s[8:9], vcc
	s_cbranch_execz .LBB0_2489
	v_add_u32_e32 v116, v141, v116
	v_ashrrev_i32_e32 v117, 31, v116
	v_readlane_b32 s10, v254, 3
	v_lshlrev_b64 v[116:117], 11, v[116:117]
	v_readlane_b32 s11, v254, 4
	v_mov_b32_e32 v155, v133
	v_mov_b32_e32 v153, v133
	v_lshl_add_u64 v[116:117], s[10:11], 0, v[116:117]
	v_lshl_add_u64 v[116:117], s[6:7], 1, v[116:117]
	v_lshl_add_u64 v[116:117], v[116:117], 0, v[154:155]
	v_lshl_add_u64 v[116:117], v[116:117], 0, v[152:153]
	v_cvt_pk_bf16_f32 v112, v112, v113
	v_cvt_pk_bf16_f32 v113, v114, v115
	v_cvt_pk_bf16_f32 v114, v108, v109
	v_cvt_pk_bf16_f32 v115, v110, v111
	v_cvt_pk_bf16_f32 v104, v104, v105
	v_cvt_pk_bf16_f32 v105, v106, v107
	v_cvt_pk_bf16_f32 v106, v100, v101
	v_cvt_pk_bf16_f32 v107, v102, v103
	s_nop 1
	v_permlane16_swap_b32 v112, v104
	v_permlane16_swap_b32 v113, v105
	v_permlane16_swap_b32 v114, v106
	v_permlane16_swap_b32 v115, v107
	global_store_dwordx4 v[116:117], v[112:115], off
	global_store_dwordx4 v[116:117], v[104:107], off offset:32
